# speedup vs baseline: 1.0185x; 1.0067x over previous
.LBB3_35:
	s_andn2_b64 vcc, exec, s[2:3]
	s_cbranch_vccnz .LBB3_39
	s_waitcnt vmcnt(4)
	v_ashrrev_i32_e32 v81, 31, v80
	v_lshl_add_u64 v[2:3], v[80:81], 3, s[20:21]
	v_add_co_u32_e32 v2, vcc, 0x48000, v2
	s_movk_i32 s8, 0x620
	s_nop 0
	v_addc_co_u32_e32 v3, vcc, 0, v3, vcc
	global_load_dwordx2 v[82:83], v[2:3], off
	v_and_b32_e32 v2, 0x70, v7
	v_bitop3_b32 v2, v0, v2, 48 bitop3:0x6c
	s_waitcnt vmcnt(4)
	v_mad_u64_u32 v[64:65], s[6:7], v9, s8, v[2:3]
	v_lshrrev_b32_e32 v3, 4, v92
	v_bitop3_b32 v3, v3, v0, 4 bitop3:0x36
	v_lshlrev_b32_e32 v3, 4, v3
	v_and_b32_e32 v4, 0x70, v3
	s_waitcnt vmcnt(3)
	v_mad_u64_u32 v[66:67], s[6:7], v8, s8, v[4:5]
	s_waitcnt vmcnt(2)
	v_mad_u64_u32 v[68:69], s[6:7], v6, s8, v[2:3]
	s_waitcnt vmcnt(1)
	v_mad_u64_u32 v[70:71], s[6:7], v1, s8, v[4:5]
	v_lshrrev_b32_e32 v85, 5, v92
	v_bfe_u32 v2, v0, 1, 3
	s_mov_b64 s[6:7], 0x1800
	s_add_u32 s4, s20, 0x4000000
	v_bitop3_b32 v32, v85, v2, 2 bitop3:0x36
	v_bitop3_b32 v33, v85, v2, 4 bitop3:0x36
	v_bitop3_b32 v34, v85, v2, 6 bitop3:0x36
	v_lshl_add_u64 v[2:3], v[86:87], 0, s[6:7]
	s_addc_u32 s5, s21, 0
	s_lshl_b32 s2, s27, 12
	s_addk_i32 s2, 0x6000
	v_lshrrev_b32_e32 v1, 1, v0
	v_or_b32_e32 v81, s2, v84
	v_lshlrev_b32_e32 v0, 7, v0
	v_and_b32_e32 v8, 0xf80, v0
	v_lshlrev_b32_e32 v9, 4, v32
	v_bitop3_b32 v1, v85, v1, 7 bitop3:0x78
	v_or3_b32 v96, s2, v9, v8
	v_lshlrev_b32_e32 v9, 4, v33
	v_lshlrev_b32_e32 v1, 4, v1
	v_or3_b32 v97, s2, v9, v8
	v_lshlrev_b32_e32 v9, 4, v34
	v_or3_b32 v95, s2, v1, v8
	v_or3_b32 v94, s2, v9, v8
	v_add_u32_e32 v98, 0x103c0, v84
	global_load_dwordx4 v[116:119], v64, s[4:5] offset:0
	global_load_dwordx4 v[120:123], v66, s[4:5] offset:0
	global_load_dwordx4 v[124:127], v68, s[4:5] offset:0
	global_load_dwordx4 v[128:131], v70, s[4:5] offset:0
	global_load_dwordx4 v[132:135], v64, s[4:5] offset:128
	global_load_dwordx4 v[136:139], v66, s[4:5] offset:128
	global_load_dwordx4 v[140:143], v68, s[4:5] offset:128
	global_load_dwordx4 v[144:147], v70, s[4:5] offset:128
	global_load_dwordx4 v[148:151], v64, s[4:5] offset:256
	global_load_dwordx4 v[152:155], v66, s[4:5] offset:256
	global_load_dwordx4 v[156:159], v68, s[4:5] offset:256
	global_load_dwordx4 v[72:75], v70, s[4:5] offset:256
	s_add_u32 m0, s46, 0x0
	s_nop 0
	global_load_lds_dwordx4 v76, s[40:41]
	s_add_u32 m0, s47, 0x0
	s_nop 0
	global_load_lds_dwordx4 v77, s[42:43]
	s_add_u32 m0, s48, 0x0
	s_nop 0
	global_load_lds_dwordx4 v78, s[44:45]
	s_add_u32 m0, s46, 0x3000
	s_add_u32 s40, s40, 0x1800
	s_addc_u32 s41, s41, 0
	global_load_lds_dwordx4 v76, s[40:41]
	s_add_u32 m0, s47, 0x3000
	s_add_u32 s42, s42, 0x1800
	s_addc_u32 s43, s43, 0
	global_load_lds_dwordx4 v77, s[42:43]
	s_add_u32 m0, s48, 0x3000
	s_add_u32 s44, s44, 0x1800
	s_addc_u32 s45, s45, 0
	global_load_lds_dwordx4 v78, s[44:45]
	s_add_u32 m0, s46, 0xd3c0
	s_add_u32 s40, s40, 0x1800
	s_addc_u32 s41, s41, 0
	global_load_lds_dwordx4 v76, s[40:41]
	s_add_u32 m0, s47, 0xd3c0
	s_add_u32 s42, s42, 0x1800
	s_addc_u32 s43, s43, 0
	global_load_lds_dwordx4 v77, s[42:43]
	s_add_u32 m0, s48, 0xd3c0
	s_add_u32 s44, s44, 0x1800
	s_addc_u32 s45, s45, 0
	global_load_lds_dwordx4 v78, s[44:45]
	s_add_u32 m0, s46, 0x103c0
	s_add_u32 s40, s40, 0x1800
	s_addc_u32 s41, s41, 0
	global_load_lds_dwordx4 v76, s[40:41]
	s_add_u32 m0, s47, 0x103c0
	s_add_u32 s42, s42, 0x1800
	s_addc_u32 s43, s43, 0
	global_load_lds_dwordx4 v77, s[42:43]
	s_add_u32 m0, s48, 0x103c0
	s_add_u32 s44, s44, 0x1800
	s_addc_u32 s45, s45, 0
	global_load_lds_dwordx4 v78, s[44:45]
	s_waitcnt vmcnt(20)
	ds_write_b128 v81, v[116:119]
	ds_write_b128 v81, v[120:123] offset:1024
	ds_write_b128 v81, v[124:127] offset:2048
	ds_write_b128 v81, v[128:131] offset:3072
	ds_read_b128 v[52:55], v95
	ds_read_b128 v[56:59], v96
	ds_read_b128 v[60:63], v97
	ds_read_b128 v[0:3], v94
	global_load_dwordx4 v[116:119], v64, s[4:5] offset:384
	global_load_dwordx4 v[120:123], v66, s[4:5] offset:384
	global_load_dwordx4 v[124:127], v68, s[4:5] offset:384
	global_load_dwordx4 v[128:131], v70, s[4:5] offset:384
	s_waitcnt vmcnt(13)
	s_waitcnt lgkmcnt(0)
	s_barrier
	ds_read_b128 v[4:7], v84 offset:0
	ds_read_b128 v[8:11], v84 offset:1024
	ds_read_b128 v[12:15], v84 offset:2048
	ds_read_b128 v[16:19], v84 offset:3072
	ds_read_b128 v[20:23], v84 offset:4096
	ds_read_b128 v[24:27], v84 offset:5120
	ds_read_b128 v[28:31], v84 offset:6144
	ds_read_b128 v[32:35], v84 offset:7168
	ds_read_b128 v[36:39], v84 offset:8192
	ds_read_b128 v[40:43], v84 offset:9216
	ds_read_b128 v[44:47], v84 offset:10240
	ds_read_b128 v[48:51], v84 offset:11264
	s_waitcnt lgkmcnt(6)
	v_mfma_f32_32x32x16_f16 a[80:95], v[4:7], v[52:55], 0
	v_mfma_f32_32x32x16_f16 a[64:79], v[8:11], v[52:55], 0
	v_mfma_f32_32x32x16_f16 a[48:63], v[12:15], v[52:55], 0
	s_waitcnt vmcnt(10)
	s_waitcnt lgkmcnt(0)
	s_barrier
	ds_read_b128 v[4:7], v84 offset:12288
	ds_read_b128 v[8:11], v84 offset:13312
	ds_read_b128 v[12:15], v84 offset:14336
	s_nop 0
	v_mfma_f32_32x32x16_f16 a[32:47], v[16:19], v[52:55], 0
	ds_read_b128 v[16:19], v84 offset:15360
	v_mfma_f32_32x32x16_f16 a[16:31], v[20:23], v[52:55], 0
	ds_read_b128 v[20:23], v84 offset:16384
	v_mfma_f32_32x32x16_f16 a[0:15], v[24:27], v[52:55], 0
	ds_read_b128 v[24:27], v84 offset:17408
	v_mfma_f32_32x32x16_f16 a[80:95], v[28:31], v[56:59], a[80:95]
	s_add_u32 m0, s46, 0x0
	s_add_u32 s40, s40, 0x1800
	s_addc_u32 s41, s41, 0
	global_load_lds_dwordx4 v76, s[40:41]
	v_mfma_f32_32x32x16_f16 a[64:79], v[32:35], v[56:59], a[64:79]
	s_add_u32 m0, s47, 0x0
	s_add_u32 s42, s42, 0x1800
	s_addc_u32 s43, s43, 0
	global_load_lds_dwordx4 v77, s[42:43]
	v_mfma_f32_32x32x16_f16 a[48:63], v[36:39], v[56:59], a[48:63]
	s_add_u32 m0, s48, 0x0
	s_add_u32 s44, s44, 0x1800
	s_addc_u32 s45, s45, 0
	global_load_lds_dwordx4 v78, s[44:45]
	v_mfma_f32_32x32x16_f16 a[32:47], v[40:43], v[56:59], a[32:47]
	v_mfma_f32_32x32x16_f16 a[16:31], v[44:47], v[56:59], a[16:31]
	v_mfma_f32_32x32x16_f16 a[0:15], v[48:51], v[56:59], a[0:15]
	ds_read_b128 v[28:31], v84 offset:18432
	ds_read_b128 v[32:35], v84 offset:19456
	ds_read_b128 v[36:39], v84 offset:20480
	ds_read_b128 v[40:43], v84 offset:21504
	ds_read_b128 v[44:47], v84 offset:22528
	ds_read_b128 v[48:51], v84 offset:23552
	s_waitcnt lgkmcnt(6)
	s_nop 0
	v_mfma_f32_32x32x16_f16 a[80:95], v[4:7], v[60:63], a[80:95]
	s_waitcnt vmcnt(23)
	ds_write_b128 v81, v[132:135]
	ds_write_b128 v81, v[136:139] offset:1024
	ds_write_b128 v81, v[140:143] offset:2048
	ds_write_b128 v81, v[144:147] offset:3072
	s_nop 0
	v_mfma_f32_32x32x16_f16 a[64:79], v[8:11], v[60:63], a[64:79]
	ds_read_b128 v[100:103], v95
	ds_read_b128 v[104:107], v96
	ds_read_b128 v[108:111], v97
	ds_read_b128 v[112:115], v94
	v_mfma_f32_32x32x16_f16 a[48:63], v[12:15], v[60:63], a[48:63]
	global_load_dwordx4 v[132:135], v64, s[4:5] offset:512
	global_load_dwordx4 v[136:139], v66, s[4:5] offset:512
	global_load_dwordx4 v[140:143], v68, s[4:5] offset:512
	global_load_dwordx4 v[144:147], v70, s[4:5] offset:512
	s_waitcnt vmcnt(14)
	s_waitcnt lgkmcnt(8)
	s_barrier
	ds_read_b128 v[4:7], v84 offset:54208
	ds_read_b128 v[8:11], v84 offset:55232
	ds_read_b128 v[12:15], v84 offset:56256
	s_nop 0
	v_mfma_f32_32x32x16_f16 a[32:47], v[16:19], v[60:63], a[32:47]
	ds_read_b128 v[16:19], v84 offset:57280
	v_mfma_f32_32x32x16_f16 a[16:31], v[20:23], v[60:63], a[16:31]
	ds_read_b128 v[20:23], v84 offset:58304
	v_mfma_f32_32x32x16_f16 a[0:15], v[24:27], v[60:63], a[0:15]
	ds_read_b128 v[24:27], v84 offset:59328
	v_mfma_f32_32x32x16_f16 a[80:95], v[28:31], v[0:3], a[80:95]
	s_add_u32 m0, s46, 0x3000
	s_add_u32 s40, s40, 0x1800
	s_addc_u32 s41, s41, 0
	global_load_lds_dwordx4 v76, s[40:41]
	s_nop 0
	v_mfma_f32_32x32x16_f16 a[64:79], v[32:35], v[0:3], a[64:79]
	s_add_u32 m0, s47, 0x3000
	s_add_u32 s42, s42, 0x1800
	s_addc_u32 s43, s43, 0
	global_load_lds_dwordx4 v77, s[42:43]
	s_nop 0
	v_mfma_f32_32x32x16_f16 a[48:63], v[36:39], v[0:3], a[48:63]
	s_add_u32 m0, s48, 0x3000
	s_add_u32 s44, s44, 0x1800
	s_addc_u32 s45, s45, 0
	global_load_lds_dwordx4 v78, s[44:45]
	s_nop 0
	v_mfma_f32_32x32x16_f16 a[32:47], v[40:43], v[0:3], a[32:47]
	v_mfma_f32_32x32x16_f16 a[16:31], v[44:47], v[0:3], a[16:31]
	v_mfma_f32_32x32x16_f16 a[0:15], v[48:51], v[0:3], a[0:15]
	s_waitcnt lgkmcnt(6)
	ds_read_b128 v[28:31], v84 offset:60352
	ds_read_b128 v[32:35], v84 offset:61376
	ds_read_b128 v[36:39], v84 offset:62400
	ds_read_b128 v[40:43], v84 offset:63424
	ds_read_b128 v[44:47], v84 offset:64448
	ds_read_b128 v[48:51], v84 offset:65472
	s_waitcnt lgkmcnt(6)
	v_mfma_f32_32x32x16_f16 a[80:95], v[4:7], v[100:103], a[80:95]
	v_mfma_f32_32x32x16_f16 a[64:79], v[8:11], v[100:103], a[64:79]
	v_mfma_f32_32x32x16_f16 a[48:63], v[12:15], v[100:103], a[48:63]
	s_waitcnt vmcnt(14)
	s_waitcnt lgkmcnt(0)
	s_barrier
	ds_read_b128 v[4:7], v98
	ds_read_b128 v[8:11], v98 offset:1024
	ds_read_b128 v[12:15], v98 offset:2048
	s_nop 0
	v_mfma_f32_32x32x16_f16 a[32:47], v[16:19], v[100:103], a[32:47]
	ds_read_b128 v[16:19], v98 offset:3072
	v_mfma_f32_32x32x16_f16 a[16:31], v[20:23], v[100:103], a[16:31]
	ds_read_b128 v[20:23], v98 offset:4096
	v_mfma_f32_32x32x16_f16 a[0:15], v[24:27], v[100:103], a[0:15]
	ds_read_b128 v[24:27], v98 offset:5120
	v_mfma_f32_32x32x16_f16 a[80:95], v[28:31], v[104:107], a[80:95]
	s_add_u32 m0, s46, 0xd3c0
	s_add_u32 s40, s40, 0x1800
	s_addc_u32 s41, s41, 0
	global_load_lds_dwordx4 v76, s[40:41]
	s_nop 0
	v_mfma_f32_32x32x16_f16 a[64:79], v[32:35], v[104:107], a[64:79]
	s_add_u32 m0, s47, 0xd3c0
	s_add_u32 s42, s42, 0x1800
	s_addc_u32 s43, s43, 0
	global_load_lds_dwordx4 v77, s[42:43]
	s_nop 0
	v_mfma_f32_32x32x16_f16 a[48:63], v[36:39], v[104:107], a[48:63]
	s_add_u32 m0, s48, 0xd3c0
	s_add_u32 s44, s44, 0x1800
	s_addc_u32 s45, s45, 0
	global_load_lds_dwordx4 v78, s[44:45]
	s_nop 0
	v_mfma_f32_32x32x16_f16 a[32:47], v[40:43], v[104:107], a[32:47]
	v_mfma_f32_32x32x16_f16 a[16:31], v[44:47], v[104:107], a[16:31]
	v_mfma_f32_32x32x16_f16 a[0:15], v[48:51], v[104:107], a[0:15]
	ds_read_b128 v[28:31], v98 offset:6144
	ds_read_b128 v[32:35], v98 offset:7168
	ds_read_b128 v[36:39], v98 offset:8192
	ds_read_b128 v[40:43], v98 offset:9216
	ds_read_b128 v[44:47], v98 offset:10240
	ds_read_b128 v[48:51], v98 offset:11264
	s_waitcnt lgkmcnt(6)
	s_nop 0
	v_mfma_f32_32x32x16_f16 a[80:95], v[4:7], v[108:111], a[80:95]
	s_waitcnt vmcnt(29)
	ds_write_b128 v81, v[148:151]
	ds_write_b128 v81, v[152:155] offset:1024
	ds_write_b128 v81, v[156:159] offset:2048
	ds_write_b128 v81, v[72:75] offset:3072
	s_nop 0
	v_mfma_f32_32x32x16_f16 a[64:79], v[8:11], v[108:111], a[64:79]
	ds_read_b128 v[52:55], v95
	ds_read_b128 v[56:59], v96
	ds_read_b128 v[60:63], v97
	ds_read_b128 v[0:3], v94
	v_mfma_f32_32x32x16_f16 a[48:63], v[12:15], v[108:111], a[48:63]
	global_load_dwordx4 v[148:151], v64, s[4:5] offset:640
	global_load_dwordx4 v[152:155], v66, s[4:5] offset:640
	global_load_dwordx4 v[156:159], v68, s[4:5] offset:640
	global_load_dwordx4 v[72:75], v70, s[4:5] offset:640
	s_waitcnt vmcnt(14)
	s_waitcnt lgkmcnt(8)
	s_barrier
	ds_read_b128 v[4:7], v84 offset:0
	ds_read_b128 v[8:11], v84 offset:1024
	ds_read_b128 v[12:15], v84 offset:2048
	s_nop 0
	v_mfma_f32_32x32x16_f16 a[32:47], v[16:19], v[108:111], a[32:47]
	ds_read_b128 v[16:19], v84 offset:3072
	v_mfma_f32_32x32x16_f16 a[16:31], v[20:23], v[108:111], a[16:31]
	ds_read_b128 v[20:23], v84 offset:4096
	v_mfma_f32_32x32x16_f16 a[0:15], v[24:27], v[108:111], a[0:15]
	ds_read_b128 v[24:27], v84 offset:5120
	v_mfma_f32_32x32x16_f16 a[80:95], v[28:31], v[112:115], a[80:95]
	s_add_u32 m0, s46, 0x103c0
	s_add_u32 s40, s40, 0x1800
	s_addc_u32 s41, s41, 0
	global_load_lds_dwordx4 v76, s[40:41]
	s_nop 0
	v_mfma_f32_32x32x16_f16 a[64:79], v[32:35], v[112:115], a[64:79]
	s_add_u32 m0, s47, 0x103c0
	s_add_u32 s42, s42, 0x1800
	s_addc_u32 s43, s43, 0
	global_load_lds_dwordx4 v77, s[42:43]
	s_nop 0
	v_mfma_f32_32x32x16_f16 a[48:63], v[36:39], v[112:115], a[48:63]
	s_add_u32 m0, s48, 0x103c0
	s_add_u32 s44, s44, 0x1800
	s_addc_u32 s45, s45, 0
	global_load_lds_dwordx4 v78, s[44:45]
	s_nop 0
	v_mfma_f32_32x32x16_f16 a[32:47], v[40:43], v[112:115], a[32:47]
	v_mfma_f32_32x32x16_f16 a[16:31], v[44:47], v[112:115], a[16:31]
	v_mfma_f32_32x32x16_f16 a[0:15], v[48:51], v[112:115], a[0:15]
	s_waitcnt lgkmcnt(6)
	ds_read_b128 v[28:31], v84 offset:6144
	ds_read_b128 v[32:35], v84 offset:7168
	ds_read_b128 v[36:39], v84 offset:8192
	ds_read_b128 v[40:43], v84 offset:9216
	ds_read_b128 v[44:47], v84 offset:10240
	ds_read_b128 v[48:51], v84 offset:11264
	s_waitcnt lgkmcnt(6)
	v_mfma_f32_32x32x16_f16 a[80:95], v[4:7], v[52:55], a[80:95]
	v_mfma_f32_32x32x16_f16 a[64:79], v[8:11], v[52:55], a[64:79]
	v_mfma_f32_32x32x16_f16 a[48:63], v[12:15], v[52:55], a[48:63]
	s_waitcnt vmcnt(10)
	s_waitcnt lgkmcnt(0)
	s_barrier
	ds_read_b128 v[4:7], v84 offset:12288
	ds_read_b128 v[8:11], v84 offset:13312
	ds_read_b128 v[12:15], v84 offset:14336
	s_nop 0
	v_mfma_f32_32x32x16_f16 a[32:47], v[16:19], v[52:55], a[32:47]
	ds_read_b128 v[16:19], v84 offset:15360
	v_mfma_f32_32x32x16_f16 a[16:31], v[20:23], v[52:55], a[16:31]
	ds_read_b128 v[20:23], v84 offset:16384
	v_mfma_f32_32x32x16_f16 a[0:15], v[24:27], v[52:55], a[0:15]
	ds_read_b128 v[24:27], v84 offset:17408
	v_mfma_f32_32x32x16_f16 a[80:95], v[28:31], v[56:59], a[80:95]
	s_add_u32 m0, s46, 0x0
	s_add_u32 s40, s40, 0x1800
	s_addc_u32 s41, s41, 0
	global_load_lds_dwordx4 v76, s[40:41]
	v_mfma_f32_32x32x16_f16 a[64:79], v[32:35], v[56:59], a[64:79]
	s_add_u32 m0, s47, 0x0
	s_add_u32 s42, s42, 0x1800
	s_addc_u32 s43, s43, 0
	global_load_lds_dwordx4 v77, s[42:43]
	v_mfma_f32_32x32x16_f16 a[48:63], v[36:39], v[56:59], a[48:63]
	s_add_u32 m0, s48, 0x0
	s_add_u32 s44, s44, 0x1800
	s_addc_u32 s45, s45, 0
	global_load_lds_dwordx4 v78, s[44:45]
	v_mfma_f32_32x32x16_f16 a[32:47], v[40:43], v[56:59], a[32:47]
	v_mfma_f32_32x32x16_f16 a[16:31], v[44:47], v[56:59], a[16:31]
	v_mfma_f32_32x32x16_f16 a[0:15], v[48:51], v[56:59], a[0:15]
	ds_read_b128 v[28:31], v84 offset:18432
	ds_read_b128 v[32:35], v84 offset:19456
	ds_read_b128 v[36:39], v84 offset:20480
	ds_read_b128 v[40:43], v84 offset:21504
	ds_read_b128 v[44:47], v84 offset:22528
	ds_read_b128 v[48:51], v84 offset:23552
	s_waitcnt lgkmcnt(6)
	s_nop 0
	v_mfma_f32_32x32x16_f16 a[80:95], v[4:7], v[60:63], a[80:95]
	s_waitcnt vmcnt(23)
	ds_write_b128 v81, v[116:119]
	ds_write_b128 v81, v[120:123] offset:1024
	ds_write_b128 v81, v[124:127] offset:2048
	ds_write_b128 v81, v[128:131] offset:3072
	s_nop 0
	v_mfma_f32_32x32x16_f16 a[64:79], v[8:11], v[60:63], a[64:79]
	ds_read_b128 v[100:103], v95
	ds_read_b128 v[104:107], v96
	ds_read_b128 v[108:111], v97
	ds_read_b128 v[112:115], v94
	v_mfma_f32_32x32x16_f16 a[48:63], v[12:15], v[60:63], a[48:63]
	global_load_dwordx4 v[116:119], v64, s[4:5] offset:768
	global_load_dwordx4 v[120:123], v66, s[4:5] offset:768
	global_load_dwordx4 v[124:127], v68, s[4:5] offset:768
	global_load_dwordx4 v[128:131], v70, s[4:5] offset:768
	s_waitcnt vmcnt(14)
	s_waitcnt lgkmcnt(8)
	s_barrier
	ds_read_b128 v[4:7], v84 offset:54208
	ds_read_b128 v[8:11], v84 offset:55232
	ds_read_b128 v[12:15], v84 offset:56256
	s_nop 0
	v_mfma_f32_32x32x16_f16 a[32:47], v[16:19], v[60:63], a[32:47]
	ds_read_b128 v[16:19], v84 offset:57280
	v_mfma_f32_32x32x16_f16 a[16:31], v[20:23], v[60:63], a[16:31]
	ds_read_b128 v[20:23], v84 offset:58304
	v_mfma_f32_32x32x16_f16 a[0:15], v[24:27], v[60:63], a[0:15]
	ds_read_b128 v[24:27], v84 offset:59328
	v_mfma_f32_32x32x16_f16 a[80:95], v[28:31], v[0:3], a[80:95]
	s_add_u32 m0, s46, 0x3000
	s_add_u32 s40, s40, 0x1800
	s_addc_u32 s41, s41, 0
	global_load_lds_dwordx4 v76, s[40:41]
	s_nop 0
	v_mfma_f32_32x32x16_f16 a[64:79], v[32:35], v[0:3], a[64:79]
	s_add_u32 m0, s47, 0x3000
	s_add_u32 s42, s42, 0x1800
	s_addc_u32 s43, s43, 0
	global_load_lds_dwordx4 v77, s[42:43]
	s_nop 0
	v_mfma_f32_32x32x16_f16 a[48:63], v[36:39], v[0:3], a[48:63]
	s_add_u32 m0, s48, 0x3000
	s_add_u32 s44, s44, 0x1800
	s_addc_u32 s45, s45, 0
	global_load_lds_dwordx4 v78, s[44:45]
	s_nop 0
	v_mfma_f32_32x32x16_f16 a[32:47], v[40:43], v[0:3], a[32:47]
	v_mfma_f32_32x32x16_f16 a[16:31], v[44:47], v[0:3], a[16:31]
	v_mfma_f32_32x32x16_f16 a[0:15], v[48:51], v[0:3], a[0:15]
	s_waitcnt lgkmcnt(6)
	ds_read_b128 v[28:31], v84 offset:60352
	ds_read_b128 v[32:35], v84 offset:61376
	ds_read_b128 v[36:39], v84 offset:62400
	ds_read_b128 v[40:43], v84 offset:63424
	ds_read_b128 v[44:47], v84 offset:64448
	ds_read_b128 v[48:51], v84 offset:65472
	s_waitcnt lgkmcnt(6)
	v_mfma_f32_32x32x16_f16 a[80:95], v[4:7], v[100:103], a[80:95]
	v_mfma_f32_32x32x16_f16 a[64:79], v[8:11], v[100:103], a[64:79]
	v_mfma_f32_32x32x16_f16 a[48:63], v[12:15], v[100:103], a[48:63]
	s_waitcnt vmcnt(10)
	s_waitcnt lgkmcnt(0)
	s_barrier
	ds_read_b128 v[4:7], v98
	ds_read_b128 v[8:11], v98 offset:1024
	ds_read_b128 v[12:15], v98 offset:2048
	s_nop 0
	v_mfma_f32_32x32x16_f16 a[32:47], v[16:19], v[100:103], a[32:47]
	ds_read_b128 v[16:19], v98 offset:3072
	v_mfma_f32_32x32x16_f16 a[16:31], v[20:23], v[100:103], a[16:31]
	ds_read_b128 v[20:23], v98 offset:4096
	v_mfma_f32_32x32x16_f16 a[0:15], v[24:27], v[100:103], a[0:15]
	ds_read_b128 v[24:27], v98 offset:5120
	v_mfma_f32_32x32x16_f16 a[80:95], v[28:31], v[104:107], a[80:95]
	s_add_u32 m0, s46, 0xd3c0
	s_add_u32 s40, s40, 0x1800
	s_addc_u32 s41, s41, 0
	global_load_lds_dwordx4 v76, s[40:41]
	s_nop 0
	v_mfma_f32_32x32x16_f16 a[64:79], v[32:35], v[104:107], a[64:79]
	s_add_u32 m0, s47, 0xd3c0
	s_add_u32 s42, s42, 0x1800
	s_addc_u32 s43, s43, 0
	global_load_lds_dwordx4 v77, s[42:43]
	s_nop 0
	v_mfma_f32_32x32x16_f16 a[48:63], v[36:39], v[104:107], a[48:63]
	s_add_u32 m0, s48, 0xd3c0
	s_add_u32 s44, s44, 0x1800
	s_addc_u32 s45, s45, 0
	global_load_lds_dwordx4 v78, s[44:45]
	s_nop 0
	v_mfma_f32_32x32x16_f16 a[32:47], v[40:43], v[104:107], a[32:47]
	v_mfma_f32_32x32x16_f16 a[16:31], v[44:47], v[104:107], a[16:31]
	v_mfma_f32_32x32x16_f16 a[0:15], v[48:51], v[104:107], a[0:15]
	ds_read_b128 v[28:31], v98 offset:6144
	ds_read_b128 v[32:35], v98 offset:7168
	ds_read_b128 v[36:39], v98 offset:8192
	ds_read_b128 v[40:43], v98 offset:9216
	ds_read_b128 v[44:47], v98 offset:10240
	ds_read_b128 v[48:51], v98 offset:11264
	s_waitcnt lgkmcnt(6)
	s_nop 0
	v_mfma_f32_32x32x16_f16 a[80:95], v[4:7], v[108:111], a[80:95]
	s_waitcnt vmcnt(26)
	ds_write_b128 v81, v[132:135]
	ds_write_b128 v81, v[136:139] offset:1024
	ds_write_b128 v81, v[140:143] offset:2048
	ds_write_b128 v81, v[144:147] offset:3072
	s_nop 0
	v_mfma_f32_32x32x16_f16 a[64:79], v[8:11], v[108:111], a[64:79]
	ds_read_b128 v[52:55], v95
	ds_read_b128 v[56:59], v96
	ds_read_b128 v[60:63], v97
	ds_read_b128 v[0:3], v94
	v_mfma_f32_32x32x16_f16 a[48:63], v[12:15], v[108:111], a[48:63]
	global_load_dwordx4 v[132:135], v64, s[4:5] offset:896
	global_load_dwordx4 v[136:139], v66, s[4:5] offset:896
	global_load_dwordx4 v[140:143], v68, s[4:5] offset:896
	global_load_dwordx4 v[144:147], v70, s[4:5] offset:896
	s_waitcnt vmcnt(14)
	s_waitcnt lgkmcnt(8)
	s_barrier
	ds_read_b128 v[4:7], v84 offset:0
	ds_read_b128 v[8:11], v84 offset:1024
	ds_read_b128 v[12:15], v84 offset:2048
	s_nop 0
	v_mfma_f32_32x32x16_f16 a[32:47], v[16:19], v[108:111], a[32:47]
	ds_read_b128 v[16:19], v84 offset:3072
	v_mfma_f32_32x32x16_f16 a[16:31], v[20:23], v[108:111], a[16:31]
	ds_read_b128 v[20:23], v84 offset:4096
	v_mfma_f32_32x32x16_f16 a[0:15], v[24:27], v[108:111], a[0:15]
	ds_read_b128 v[24:27], v84 offset:5120
	v_mfma_f32_32x32x16_f16 a[80:95], v[28:31], v[112:115], a[80:95]
	s_add_u32 m0, s46, 0x103c0
	s_add_u32 s40, s40, 0x1800
	s_addc_u32 s41, s41, 0
	global_load_lds_dwordx4 v76, s[40:41]
	s_nop 0
	v_mfma_f32_32x32x16_f16 a[64:79], v[32:35], v[112:115], a[64:79]
	s_add_u32 m0, s47, 0x103c0
	s_add_u32 s42, s42, 0x1800
	s_addc_u32 s43, s43, 0
	global_load_lds_dwordx4 v77, s[42:43]
	s_nop 0
	v_mfma_f32_32x32x16_f16 a[48:63], v[36:39], v[112:115], a[48:63]
	s_add_u32 m0, s48, 0x103c0
	s_add_u32 s44, s44, 0x1800
	s_addc_u32 s45, s45, 0
	global_load_lds_dwordx4 v78, s[44:45]
	s_nop 0
	v_mfma_f32_32x32x16_f16 a[32:47], v[40:43], v[112:115], a[32:47]
	v_mfma_f32_32x32x16_f16 a[16:31], v[44:47], v[112:115], a[16:31]
	v_mfma_f32_32x32x16_f16 a[0:15], v[48:51], v[112:115], a[0:15]
	s_waitcnt lgkmcnt(6)
	ds_read_b128 v[28:31], v84 offset:6144
	ds_read_b128 v[32:35], v84 offset:7168
	ds_read_b128 v[36:39], v84 offset:8192
	ds_read_b128 v[40:43], v84 offset:9216
	ds_read_b128 v[44:47], v84 offset:10240
	ds_read_b128 v[48:51], v84 offset:11264
	s_waitcnt lgkmcnt(6)
	v_mfma_f32_32x32x16_f16 a[80:95], v[4:7], v[52:55], a[80:95]
	v_mfma_f32_32x32x16_f16 a[64:79], v[8:11], v[52:55], a[64:79]
	v_mfma_f32_32x32x16_f16 a[48:63], v[12:15], v[52:55], a[48:63]
	s_waitcnt vmcnt(10)
	s_waitcnt lgkmcnt(0)
	s_barrier
	ds_read_b128 v[4:7], v84 offset:12288
	ds_read_b128 v[8:11], v84 offset:13312
	ds_read_b128 v[12:15], v84 offset:14336
	s_nop 0
	v_mfma_f32_32x32x16_f16 a[32:47], v[16:19], v[52:55], a[32:47]
	ds_read_b128 v[16:19], v84 offset:15360
	v_mfma_f32_32x32x16_f16 a[16:31], v[20:23], v[52:55], a[16:31]
	ds_read_b128 v[20:23], v84 offset:16384
	v_mfma_f32_32x32x16_f16 a[0:15], v[24:27], v[52:55], a[0:15]
	ds_read_b128 v[24:27], v84 offset:17408
	v_mfma_f32_32x32x16_f16 a[80:95], v[28:31], v[56:59], a[80:95]
	s_add_u32 m0, s46, 0x0
	s_add_u32 s40, s40, 0x1800
	s_addc_u32 s41, s41, 0
	global_load_lds_dwordx4 v76, s[40:41]
	v_mfma_f32_32x32x16_f16 a[64:79], v[32:35], v[56:59], a[64:79]
	s_add_u32 m0, s47, 0x0
	s_add_u32 s42, s42, 0x1800
	s_addc_u32 s43, s43, 0
	global_load_lds_dwordx4 v77, s[42:43]
	v_mfma_f32_32x32x16_f16 a[48:63], v[36:39], v[56:59], a[48:63]
	s_add_u32 m0, s48, 0x0
	s_add_u32 s44, s44, 0x1800
	s_addc_u32 s45, s45, 0
	global_load_lds_dwordx4 v78, s[44:45]
	v_mfma_f32_32x32x16_f16 a[32:47], v[40:43], v[56:59], a[32:47]
	v_mfma_f32_32x32x16_f16 a[16:31], v[44:47], v[56:59], a[16:31]
	v_mfma_f32_32x32x16_f16 a[0:15], v[48:51], v[56:59], a[0:15]
	ds_read_b128 v[28:31], v84 offset:18432
	ds_read_b128 v[32:35], v84 offset:19456
	ds_read_b128 v[36:39], v84 offset:20480
	ds_read_b128 v[40:43], v84 offset:21504
	ds_read_b128 v[44:47], v84 offset:22528
	ds_read_b128 v[48:51], v84 offset:23552
	s_waitcnt lgkmcnt(6)
	s_nop 0
	v_mfma_f32_32x32x16_f16 a[80:95], v[4:7], v[60:63], a[80:95]
	s_waitcnt vmcnt(26)
	ds_write_b128 v81, v[148:151]
	ds_write_b128 v81, v[152:155] offset:1024
	ds_write_b128 v81, v[156:159] offset:2048
	ds_write_b128 v81, v[72:75] offset:3072
	s_nop 0
	v_mfma_f32_32x32x16_f16 a[64:79], v[8:11], v[60:63], a[64:79]
	ds_read_b128 v[100:103], v95
	ds_read_b128 v[104:107], v96
	ds_read_b128 v[108:111], v97
	ds_read_b128 v[112:115], v94
	v_mfma_f32_32x32x16_f16 a[48:63], v[12:15], v[60:63], a[48:63]
	global_load_dwordx4 v[148:151], v64, s[4:5] offset:1024
	global_load_dwordx4 v[152:155], v66, s[4:5] offset:1024
	global_load_dwordx4 v[156:159], v68, s[4:5] offset:1024
	global_load_dwordx4 v[72:75], v70, s[4:5] offset:1024
	s_waitcnt vmcnt(14)
	s_waitcnt lgkmcnt(8)
	s_barrier
	ds_read_b128 v[4:7], v84 offset:54208
	ds_read_b128 v[8:11], v84 offset:55232
	ds_read_b128 v[12:15], v84 offset:56256
	s_nop 0
	v_mfma_f32_32x32x16_f16 a[32:47], v[16:19], v[60:63], a[32:47]
	ds_read_b128 v[16:19], v84 offset:57280
	v_mfma_f32_32x32x16_f16 a[16:31], v[20:23], v[60:63], a[16:31]
	ds_read_b128 v[20:23], v84 offset:58304
	v_mfma_f32_32x32x16_f16 a[0:15], v[24:27], v[60:63], a[0:15]
	ds_read_b128 v[24:27], v84 offset:59328
	v_mfma_f32_32x32x16_f16 a[80:95], v[28:31], v[0:3], a[80:95]
	s_add_u32 m0, s46, 0x3000
	s_add_u32 s40, s40, 0x1800
	s_addc_u32 s41, s41, 0
	global_load_lds_dwordx4 v76, s[40:41]
	s_nop 0
	v_mfma_f32_32x32x16_f16 a[64:79], v[32:35], v[0:3], a[64:79]
	s_add_u32 m0, s47, 0x3000
	s_add_u32 s42, s42, 0x1800
	s_addc_u32 s43, s43, 0
	global_load_lds_dwordx4 v77, s[42:43]
	s_nop 0
	v_mfma_f32_32x32x16_f16 a[48:63], v[36:39], v[0:3], a[48:63]
	s_add_u32 m0, s48, 0x3000
	s_add_u32 s44, s44, 0x1800
	s_addc_u32 s45, s45, 0
	global_load_lds_dwordx4 v78, s[44:45]
	s_nop 0
	v_mfma_f32_32x32x16_f16 a[32:47], v[40:43], v[0:3], a[32:47]
	v_mfma_f32_32x32x16_f16 a[16:31], v[44:47], v[0:3], a[16:31]
	v_mfma_f32_32x32x16_f16 a[0:15], v[48:51], v[0:3], a[0:15]
	s_waitcnt lgkmcnt(6)
	ds_read_b128 v[28:31], v84 offset:60352
	ds_read_b128 v[32:35], v84 offset:61376
	ds_read_b128 v[36:39], v84 offset:62400
	ds_read_b128 v[40:43], v84 offset:63424
	ds_read_b128 v[44:47], v84 offset:64448
	ds_read_b128 v[48:51], v84 offset:65472
	s_waitcnt lgkmcnt(6)
	v_mfma_f32_32x32x16_f16 a[80:95], v[4:7], v[100:103], a[80:95]
	v_mfma_f32_32x32x16_f16 a[64:79], v[8:11], v[100:103], a[64:79]
	v_mfma_f32_32x32x16_f16 a[48:63], v[12:15], v[100:103], a[48:63]
	s_waitcnt vmcnt(10)
	s_waitcnt lgkmcnt(0)
	s_barrier
	ds_read_b128 v[4:7], v98
	ds_read_b128 v[8:11], v98 offset:1024
	ds_read_b128 v[12:15], v98 offset:2048
	s_nop 0
	v_mfma_f32_32x32x16_f16 a[32:47], v[16:19], v[100:103], a[32:47]
	ds_read_b128 v[16:19], v98 offset:3072
	v_mfma_f32_32x32x16_f16 a[16:31], v[20:23], v[100:103], a[16:31]
	ds_read_b128 v[20:23], v98 offset:4096
	v_mfma_f32_32x32x16_f16 a[0:15], v[24:27], v[100:103], a[0:15]
	ds_read_b128 v[24:27], v98 offset:5120
	v_mfma_f32_32x32x16_f16 a[80:95], v[28:31], v[104:107], a[80:95]
	s_add_u32 m0, s46, 0xd3c0
	s_add_u32 s40, s40, 0x1800
	s_addc_u32 s41, s41, 0
	global_load_lds_dwordx4 v76, s[40:41]
	s_nop 0
	v_mfma_f32_32x32x16_f16 a[64:79], v[32:35], v[104:107], a[64:79]
	s_add_u32 m0, s47, 0xd3c0
	s_add_u32 s42, s42, 0x1800
	s_addc_u32 s43, s43, 0
	global_load_lds_dwordx4 v77, s[42:43]
	s_nop 0
	v_mfma_f32_32x32x16_f16 a[48:63], v[36:39], v[104:107], a[48:63]
	s_add_u32 m0, s48, 0xd3c0
	s_add_u32 s44, s44, 0x1800
	s_addc_u32 s45, s45, 0
	global_load_lds_dwordx4 v78, s[44:45]
	s_nop 0
	v_mfma_f32_32x32x16_f16 a[32:47], v[40:43], v[104:107], a[32:47]
	v_mfma_f32_32x32x16_f16 a[16:31], v[44:47], v[104:107], a[16:31]
	v_mfma_f32_32x32x16_f16 a[0:15], v[48:51], v[104:107], a[0:15]
	ds_read_b128 v[28:31], v98 offset:6144
	ds_read_b128 v[32:35], v98 offset:7168
	ds_read_b128 v[36:39], v98 offset:8192
	ds_read_b128 v[40:43], v98 offset:9216
	ds_read_b128 v[44:47], v98 offset:10240
	ds_read_b128 v[48:51], v98 offset:11264
	s_waitcnt lgkmcnt(6)
	s_nop 0
	v_mfma_f32_32x32x16_f16 a[80:95], v[4:7], v[108:111], a[80:95]
	s_waitcnt vmcnt(26)
	ds_write_b128 v81, v[116:119]
	ds_write_b128 v81, v[120:123] offset:1024
	ds_write_b128 v81, v[124:127] offset:2048
	ds_write_b128 v81, v[128:131] offset:3072
	s_nop 0
	v_mfma_f32_32x32x16_f16 a[64:79], v[8:11], v[108:111], a[64:79]
	ds_read_b128 v[52:55], v95
	ds_read_b128 v[56:59], v96
	ds_read_b128 v[60:63], v97
	ds_read_b128 v[0:3], v94
	v_mfma_f32_32x32x16_f16 a[48:63], v[12:15], v[108:111], a[48:63]
	global_load_dwordx4 v[116:119], v64, s[4:5] offset:1152
	global_load_dwordx4 v[120:123], v66, s[4:5] offset:1152
	global_load_dwordx4 v[124:127], v68, s[4:5] offset:1152
	global_load_dwordx4 v[128:131], v70, s[4:5] offset:1152
	s_waitcnt vmcnt(14)
	s_waitcnt lgkmcnt(8)
	s_barrier
	ds_read_b128 v[4:7], v84 offset:0
	ds_read_b128 v[8:11], v84 offset:1024
	ds_read_b128 v[12:15], v84 offset:2048
	s_nop 0
	v_mfma_f32_32x32x16_f16 a[32:47], v[16:19], v[108:111], a[32:47]
	ds_read_b128 v[16:19], v84 offset:3072
	v_mfma_f32_32x32x16_f16 a[16:31], v[20:23], v[108:111], a[16:31]
	ds_read_b128 v[20:23], v84 offset:4096
	v_mfma_f32_32x32x16_f16 a[0:15], v[24:27], v[108:111], a[0:15]
	ds_read_b128 v[24:27], v84 offset:5120
	v_mfma_f32_32x32x16_f16 a[80:95], v[28:31], v[112:115], a[80:95]
	s_add_u32 m0, s46, 0x103c0
	s_add_u32 s40, s40, 0x1800
	s_addc_u32 s41, s41, 0
	global_load_lds_dwordx4 v76, s[40:41]
	s_nop 0
	v_mfma_f32_32x32x16_f16 a[64:79], v[32:35], v[112:115], a[64:79]
	s_add_u32 m0, s47, 0x103c0
	s_add_u32 s42, s42, 0x1800
	s_addc_u32 s43, s43, 0
	global_load_lds_dwordx4 v77, s[42:43]
	s_nop 0
	v_mfma_f32_32x32x16_f16 a[48:63], v[36:39], v[112:115], a[48:63]
	s_add_u32 m0, s48, 0x103c0
	s_add_u32 s44, s44, 0x1800
	s_addc_u32 s45, s45, 0
	global_load_lds_dwordx4 v78, s[44:45]
	s_nop 0
	v_mfma_f32_32x32x16_f16 a[32:47], v[40:43], v[112:115], a[32:47]
	v_mfma_f32_32x32x16_f16 a[16:31], v[44:47], v[112:115], a[16:31]
	v_mfma_f32_32x32x16_f16 a[0:15], v[48:51], v[112:115], a[0:15]
	s_waitcnt lgkmcnt(6)
	ds_read_b128 v[28:31], v84 offset:6144
	ds_read_b128 v[32:35], v84 offset:7168
	ds_read_b128 v[36:39], v84 offset:8192
	ds_read_b128 v[40:43], v84 offset:9216
	ds_read_b128 v[44:47], v84 offset:10240
	ds_read_b128 v[48:51], v84 offset:11264
	s_waitcnt lgkmcnt(6)
	v_mfma_f32_32x32x16_f16 a[80:95], v[4:7], v[52:55], a[80:95]
	v_mfma_f32_32x32x16_f16 a[64:79], v[8:11], v[52:55], a[64:79]
	v_mfma_f32_32x32x16_f16 a[48:63], v[12:15], v[52:55], a[48:63]
	s_waitcnt vmcnt(10)
	s_waitcnt lgkmcnt(0)
	s_barrier
	ds_read_b128 v[4:7], v84 offset:12288
	ds_read_b128 v[8:11], v84 offset:13312
	ds_read_b128 v[12:15], v84 offset:14336
	s_nop 0
	v_mfma_f32_32x32x16_f16 a[32:47], v[16:19], v[52:55], a[32:47]
	ds_read_b128 v[16:19], v84 offset:15360
	v_mfma_f32_32x32x16_f16 a[16:31], v[20:23], v[52:55], a[16:31]
	ds_read_b128 v[20:23], v84 offset:16384
	v_mfma_f32_32x32x16_f16 a[0:15], v[24:27], v[52:55], a[0:15]
	ds_read_b128 v[24:27], v84 offset:17408
	v_mfma_f32_32x32x16_f16 a[80:95], v[28:31], v[56:59], a[80:95]
	s_add_u32 m0, s46, 0x0
	s_add_u32 s40, s40, 0x1800
	s_addc_u32 s41, s41, 0
	global_load_lds_dwordx4 v76, s[40:41]
	v_mfma_f32_32x32x16_f16 a[64:79], v[32:35], v[56:59], a[64:79]
	s_add_u32 m0, s47, 0x0
	s_add_u32 s42, s42, 0x1800
	s_addc_u32 s43, s43, 0
	global_load_lds_dwordx4 v77, s[42:43]
	v_mfma_f32_32x32x16_f16 a[48:63], v[36:39], v[56:59], a[48:63]
	s_add_u32 m0, s48, 0x0
	s_add_u32 s44, s44, 0x1800
	s_addc_u32 s45, s45, 0
	global_load_lds_dwordx4 v78, s[44:45]
	v_mfma_f32_32x32x16_f16 a[32:47], v[40:43], v[56:59], a[32:47]
	v_mfma_f32_32x32x16_f16 a[16:31], v[44:47], v[56:59], a[16:31]
	v_mfma_f32_32x32x16_f16 a[0:15], v[48:51], v[56:59], a[0:15]
	ds_read_b128 v[28:31], v84 offset:18432
	ds_read_b128 v[32:35], v84 offset:19456
	ds_read_b128 v[36:39], v84 offset:20480
	ds_read_b128 v[40:43], v84 offset:21504
	ds_read_b128 v[44:47], v84 offset:22528
	ds_read_b128 v[48:51], v84 offset:23552
	s_waitcnt lgkmcnt(6)
	s_nop 0
	v_mfma_f32_32x32x16_f16 a[80:95], v[4:7], v[60:63], a[80:95]
	s_waitcnt vmcnt(26)
	ds_write_b128 v81, v[132:135]
	ds_write_b128 v81, v[136:139] offset:1024
	ds_write_b128 v81, v[140:143] offset:2048
	ds_write_b128 v81, v[144:147] offset:3072
	s_nop 0
	v_mfma_f32_32x32x16_f16 a[64:79], v[8:11], v[60:63], a[64:79]
	ds_read_b128 v[100:103], v95
	ds_read_b128 v[104:107], v96
	ds_read_b128 v[108:111], v97
	ds_read_b128 v[112:115], v94
	v_mfma_f32_32x32x16_f16 a[48:63], v[12:15], v[60:63], a[48:63]
	global_load_dwordx4 v[132:135], v64, s[4:5] offset:1280
	global_load_dwordx4 v[136:139], v66, s[4:5] offset:1280
	global_load_dwordx4 v[140:143], v68, s[4:5] offset:1280
	global_load_dwordx4 v[144:147], v70, s[4:5] offset:1280
	s_waitcnt vmcnt(14)
	s_waitcnt lgkmcnt(8)
	s_barrier
	ds_read_b128 v[4:7], v84 offset:54208
	ds_read_b128 v[8:11], v84 offset:55232
	ds_read_b128 v[12:15], v84 offset:56256
	s_nop 0
	v_mfma_f32_32x32x16_f16 a[32:47], v[16:19], v[60:63], a[32:47]
	ds_read_b128 v[16:19], v84 offset:57280
	v_mfma_f32_32x32x16_f16 a[16:31], v[20:23], v[60:63], a[16:31]
	ds_read_b128 v[20:23], v84 offset:58304
	v_mfma_f32_32x32x16_f16 a[0:15], v[24:27], v[60:63], a[0:15]
	ds_read_b128 v[24:27], v84 offset:59328
	v_mfma_f32_32x32x16_f16 a[80:95], v[28:31], v[0:3], a[80:95]
	s_add_u32 m0, s46, 0x3000
	s_add_u32 s40, s40, 0x1800
	s_addc_u32 s41, s41, 0
	global_load_lds_dwordx4 v76, s[40:41]
	s_nop 0
	v_mfma_f32_32x32x16_f16 a[64:79], v[32:35], v[0:3], a[64:79]
	s_add_u32 m0, s47, 0x3000
	s_add_u32 s42, s42, 0x1800
	s_addc_u32 s43, s43, 0
	global_load_lds_dwordx4 v77, s[42:43]
	s_nop 0
	v_mfma_f32_32x32x16_f16 a[48:63], v[36:39], v[0:3], a[48:63]
	s_add_u32 m0, s48, 0x3000
	s_add_u32 s44, s44, 0x1800
	s_addc_u32 s45, s45, 0
	global_load_lds_dwordx4 v78, s[44:45]
	s_nop 0
	v_mfma_f32_32x32x16_f16 a[32:47], v[40:43], v[0:3], a[32:47]
	v_mfma_f32_32x32x16_f16 a[16:31], v[44:47], v[0:3], a[16:31]
	v_mfma_f32_32x32x16_f16 a[0:15], v[48:51], v[0:3], a[0:15]
	s_waitcnt lgkmcnt(6)
	ds_read_b128 v[28:31], v84 offset:60352
	ds_read_b128 v[32:35], v84 offset:61376
	ds_read_b128 v[36:39], v84 offset:62400
	ds_read_b128 v[40:43], v84 offset:63424
	ds_read_b128 v[44:47], v84 offset:64448
	ds_read_b128 v[48:51], v84 offset:65472
	s_waitcnt lgkmcnt(6)
	v_mfma_f32_32x32x16_f16 a[80:95], v[4:7], v[100:103], a[80:95]
	v_mfma_f32_32x32x16_f16 a[64:79], v[8:11], v[100:103], a[64:79]
	v_mfma_f32_32x32x16_f16 a[48:63], v[12:15], v[100:103], a[48:63]
	s_waitcnt vmcnt(10)
	s_waitcnt lgkmcnt(0)
	s_barrier
	ds_read_b128 v[4:7], v98
	ds_read_b128 v[8:11], v98 offset:1024
	ds_read_b128 v[12:15], v98 offset:2048
	s_nop 0
	v_mfma_f32_32x32x16_f16 a[32:47], v[16:19], v[100:103], a[32:47]
	ds_read_b128 v[16:19], v98 offset:3072
	v_mfma_f32_32x32x16_f16 a[16:31], v[20:23], v[100:103], a[16:31]
	ds_read_b128 v[20:23], v98 offset:4096
	v_mfma_f32_32x32x16_f16 a[0:15], v[24:27], v[100:103], a[0:15]
	ds_read_b128 v[24:27], v98 offset:5120
	v_mfma_f32_32x32x16_f16 a[80:95], v[28:31], v[104:107], a[80:95]
	s_add_u32 m0, s46, 0xd3c0
	s_add_u32 s40, s40, 0x1800
	s_addc_u32 s41, s41, 0
	global_load_lds_dwordx4 v76, s[40:41]
	s_nop 0
	v_mfma_f32_32x32x16_f16 a[64:79], v[32:35], v[104:107], a[64:79]
	s_add_u32 m0, s47, 0xd3c0
	s_add_u32 s42, s42, 0x1800
	s_addc_u32 s43, s43, 0
	global_load_lds_dwordx4 v77, s[42:43]
	s_nop 0
	v_mfma_f32_32x32x16_f16 a[48:63], v[36:39], v[104:107], a[48:63]
	s_add_u32 m0, s48, 0xd3c0
	s_add_u32 s44, s44, 0x1800
	s_addc_u32 s45, s45, 0
	global_load_lds_dwordx4 v78, s[44:45]
	s_nop 0
	v_mfma_f32_32x32x16_f16 a[32:47], v[40:43], v[104:107], a[32:47]
	v_mfma_f32_32x32x16_f16 a[16:31], v[44:47], v[104:107], a[16:31]
	v_mfma_f32_32x32x16_f16 a[0:15], v[48:51], v[104:107], a[0:15]
	ds_read_b128 v[28:31], v98 offset:6144
	ds_read_b128 v[32:35], v98 offset:7168
	ds_read_b128 v[36:39], v98 offset:8192
	ds_read_b128 v[40:43], v98 offset:9216
	ds_read_b128 v[44:47], v98 offset:10240
	ds_read_b128 v[48:51], v98 offset:11264
	s_waitcnt lgkmcnt(6)
	s_nop 0
	v_mfma_f32_32x32x16_f16 a[80:95], v[4:7], v[108:111], a[80:95]
	s_waitcnt vmcnt(26)
	ds_write_b128 v81, v[148:151]
	ds_write_b128 v81, v[152:155] offset:1024
	ds_write_b128 v81, v[156:159] offset:2048
	ds_write_b128 v81, v[72:75] offset:3072
	s_nop 0
	v_mfma_f32_32x32x16_f16 a[64:79], v[8:11], v[108:111], a[64:79]
	ds_read_b128 v[52:55], v95
	ds_read_b128 v[56:59], v96
	ds_read_b128 v[60:63], v97
	ds_read_b128 v[0:3], v94
	v_mfma_f32_32x32x16_f16 a[48:63], v[12:15], v[108:111], a[48:63]
	global_load_dwordx4 v[148:151], v64, s[4:5] offset:1408
	global_load_dwordx4 v[152:155], v66, s[4:5] offset:1408
	global_load_dwordx4 v[156:159], v68, s[4:5] offset:1408
	global_load_dwordx4 v[72:75], v70, s[4:5] offset:1408
	s_waitcnt vmcnt(14)
	s_waitcnt lgkmcnt(8)
	s_barrier
	ds_read_b128 v[4:7], v84 offset:0
	ds_read_b128 v[8:11], v84 offset:1024
	ds_read_b128 v[12:15], v84 offset:2048
	s_nop 0
	v_mfma_f32_32x32x16_f16 a[32:47], v[16:19], v[108:111], a[32:47]
	ds_read_b128 v[16:19], v84 offset:3072
	v_mfma_f32_32x32x16_f16 a[16:31], v[20:23], v[108:111], a[16:31]
	ds_read_b128 v[20:23], v84 offset:4096
	v_mfma_f32_32x32x16_f16 a[0:15], v[24:27], v[108:111], a[0:15]
	ds_read_b128 v[24:27], v84 offset:5120
	v_mfma_f32_32x32x16_f16 a[80:95], v[28:31], v[112:115], a[80:95]
	s_add_u32 m0, s46, 0x103c0
	s_add_u32 s40, s40, 0x1800
	s_addc_u32 s41, s41, 0
	global_load_lds_dwordx4 v76, s[40:41]
	s_nop 0
	v_mfma_f32_32x32x16_f16 a[64:79], v[32:35], v[112:115], a[64:79]
	s_add_u32 m0, s47, 0x103c0
	s_add_u32 s42, s42, 0x1800
	s_addc_u32 s43, s43, 0
	global_load_lds_dwordx4 v77, s[42:43]
	s_nop 0
	v_mfma_f32_32x32x16_f16 a[48:63], v[36:39], v[112:115], a[48:63]
	s_add_u32 m0, s48, 0x103c0
	s_add_u32 s44, s44, 0x1800
	s_addc_u32 s45, s45, 0
	global_load_lds_dwordx4 v78, s[44:45]
	s_nop 0
	v_mfma_f32_32x32x16_f16 a[32:47], v[40:43], v[112:115], a[32:47]
	v_mfma_f32_32x32x16_f16 a[16:31], v[44:47], v[112:115], a[16:31]
	v_mfma_f32_32x32x16_f16 a[0:15], v[48:51], v[112:115], a[0:15]
	s_waitcnt lgkmcnt(6)
	ds_read_b128 v[28:31], v84 offset:6144
	ds_read_b128 v[32:35], v84 offset:7168
	ds_read_b128 v[36:39], v84 offset:8192
	ds_read_b128 v[40:43], v84 offset:9216
	ds_read_b128 v[44:47], v84 offset:10240
	ds_read_b128 v[48:51], v84 offset:11264
	s_waitcnt lgkmcnt(6)
	v_mfma_f32_32x32x16_f16 a[80:95], v[4:7], v[52:55], a[80:95]
	v_mfma_f32_32x32x16_f16 a[64:79], v[8:11], v[52:55], a[64:79]
	v_mfma_f32_32x32x16_f16 a[48:63], v[12:15], v[52:55], a[48:63]
	s_waitcnt vmcnt(10)
	s_waitcnt lgkmcnt(0)
	s_barrier
	ds_read_b128 v[4:7], v84 offset:12288
	ds_read_b128 v[8:11], v84 offset:13312
	ds_read_b128 v[12:15], v84 offset:14336
	s_nop 0
	v_mfma_f32_32x32x16_f16 a[32:47], v[16:19], v[52:55], a[32:47]
	ds_read_b128 v[16:19], v84 offset:15360
	v_mfma_f32_32x32x16_f16 a[16:31], v[20:23], v[52:55], a[16:31]
	ds_read_b128 v[20:23], v84 offset:16384
	v_mfma_f32_32x32x16_f16 a[0:15], v[24:27], v[52:55], a[0:15]
	ds_read_b128 v[24:27], v84 offset:17408
	v_mfma_f32_32x32x16_f16 a[80:95], v[28:31], v[56:59], a[80:95]
	s_add_u32 m0, s46, 0x0
	s_add_u32 s40, s40, 0x1800
	s_addc_u32 s41, s41, 0
	global_load_lds_dwordx4 v76, s[40:41]
	v_mfma_f32_32x32x16_f16 a[64:79], v[32:35], v[56:59], a[64:79]
	s_add_u32 m0, s47, 0x0
	s_add_u32 s42, s42, 0x1800
	s_addc_u32 s43, s43, 0
	global_load_lds_dwordx4 v77, s[42:43]
	v_mfma_f32_32x32x16_f16 a[48:63], v[36:39], v[56:59], a[48:63]
	s_add_u32 m0, s48, 0x0
	s_add_u32 s44, s44, 0x1800
	s_addc_u32 s45, s45, 0
	global_load_lds_dwordx4 v78, s[44:45]
	v_mfma_f32_32x32x16_f16 a[32:47], v[40:43], v[56:59], a[32:47]
	v_mfma_f32_32x32x16_f16 a[16:31], v[44:47], v[56:59], a[16:31]
	v_mfma_f32_32x32x16_f16 a[0:15], v[48:51], v[56:59], a[0:15]
	ds_read_b128 v[28:31], v84 offset:18432
	ds_read_b128 v[32:35], v84 offset:19456
	ds_read_b128 v[36:39], v84 offset:20480
	ds_read_b128 v[40:43], v84 offset:21504
	ds_read_b128 v[44:47], v84 offset:22528
	ds_read_b128 v[48:51], v84 offset:23552
	s_waitcnt lgkmcnt(6)
	s_nop 0
	v_mfma_f32_32x32x16_f16 a[80:95], v[4:7], v[60:63], a[80:95]
	s_waitcnt vmcnt(26)
	ds_write_b128 v81, v[116:119]
	ds_write_b128 v81, v[120:123] offset:1024
	ds_write_b128 v81, v[124:127] offset:2048
	ds_write_b128 v81, v[128:131] offset:3072
	s_nop 0
	v_mfma_f32_32x32x16_f16 a[64:79], v[8:11], v[60:63], a[64:79]
	ds_read_b128 v[100:103], v95
	ds_read_b128 v[104:107], v96
	ds_read_b128 v[108:111], v97
	ds_read_b128 v[112:115], v94
	v_mfma_f32_32x32x16_f16 a[48:63], v[12:15], v[60:63], a[48:63]
	global_load_dwordx4 v[116:119], v64, s[4:5] offset:1440
	global_load_dwordx4 v[120:123], v66, s[4:5] offset:1440
	global_load_dwordx4 v[124:127], v68, s[4:5] offset:1440
	global_load_dwordx4 v[128:131], v70, s[4:5] offset:1440
	s_waitcnt vmcnt(14)
	s_waitcnt lgkmcnt(8)
	s_barrier
	ds_read_b128 v[4:7], v84 offset:54208
	ds_read_b128 v[8:11], v84 offset:55232
	ds_read_b128 v[12:15], v84 offset:56256
	s_nop 0
	v_mfma_f32_32x32x16_f16 a[32:47], v[16:19], v[60:63], a[32:47]
	ds_read_b128 v[16:19], v84 offset:57280
	v_mfma_f32_32x32x16_f16 a[16:31], v[20:23], v[60:63], a[16:31]
	ds_read_b128 v[20:23], v84 offset:58304
	v_mfma_f32_32x32x16_f16 a[0:15], v[24:27], v[60:63], a[0:15]
	ds_read_b128 v[24:27], v84 offset:59328
	v_mfma_f32_32x32x16_f16 a[80:95], v[28:31], v[0:3], a[80:95]
	s_add_u32 m0, s46, 0x3000
	s_add_u32 s40, s40, 0x1800
	s_addc_u32 s41, s41, 0
	global_load_lds_dwordx4 v76, s[40:41]
	s_nop 0
	v_mfma_f32_32x32x16_f16 a[64:79], v[32:35], v[0:3], a[64:79]
	s_add_u32 m0, s47, 0x3000
	s_add_u32 s42, s42, 0x1800
	s_addc_u32 s43, s43, 0
	global_load_lds_dwordx4 v77, s[42:43]
	s_nop 0
	v_mfma_f32_32x32x16_f16 a[48:63], v[36:39], v[0:3], a[48:63]
	s_add_u32 m0, s48, 0x3000
	s_add_u32 s44, s44, 0x1800
	s_addc_u32 s45, s45, 0
	global_load_lds_dwordx4 v78, s[44:45]
	s_nop 0
	v_mfma_f32_32x32x16_f16 a[32:47], v[40:43], v[0:3], a[32:47]
	v_mfma_f32_32x32x16_f16 a[16:31], v[44:47], v[0:3], a[16:31]
	v_mfma_f32_32x32x16_f16 a[0:15], v[48:51], v[0:3], a[0:15]
	s_waitcnt lgkmcnt(6)
	ds_read_b128 v[28:31], v84 offset:60352
	ds_read_b128 v[32:35], v84 offset:61376
	ds_read_b128 v[36:39], v84 offset:62400
	ds_read_b128 v[40:43], v84 offset:63424
	ds_read_b128 v[44:47], v84 offset:64448
	ds_read_b128 v[48:51], v84 offset:65472
	s_waitcnt lgkmcnt(6)
	v_mfma_f32_32x32x16_f16 a[80:95], v[4:7], v[100:103], a[80:95]
	v_mfma_f32_32x32x16_f16 a[64:79], v[8:11], v[100:103], a[64:79]
	v_mfma_f32_32x32x16_f16 a[48:63], v[12:15], v[100:103], a[48:63]
	s_waitcnt vmcnt(10)
	s_waitcnt lgkmcnt(0)
	s_barrier
	ds_read_b128 v[4:7], v98
	ds_read_b128 v[8:11], v98 offset:1024
	ds_read_b128 v[12:15], v98 offset:2048
	s_nop 0
	v_mfma_f32_32x32x16_f16 a[32:47], v[16:19], v[100:103], a[32:47]
	ds_read_b128 v[16:19], v98 offset:3072
	v_mfma_f32_32x32x16_f16 a[16:31], v[20:23], v[100:103], a[16:31]
	ds_read_b128 v[20:23], v98 offset:4096
	v_mfma_f32_32x32x16_f16 a[0:15], v[24:27], v[100:103], a[0:15]
	ds_read_b128 v[24:27], v98 offset:5120
	v_mfma_f32_32x32x16_f16 a[80:95], v[28:31], v[104:107], a[80:95]
	s_add_u32 m0, s46, 0xd3c0
	s_add_u32 s40, s40, 0x1800
	s_addc_u32 s41, s41, 0
	global_load_lds_dwordx4 v76, s[40:41]
	s_nop 0
	v_mfma_f32_32x32x16_f16 a[64:79], v[32:35], v[104:107], a[64:79]
	s_add_u32 m0, s47, 0xd3c0
	s_add_u32 s42, s42, 0x1800
	s_addc_u32 s43, s43, 0
	global_load_lds_dwordx4 v77, s[42:43]
	s_nop 0
	v_mfma_f32_32x32x16_f16 a[48:63], v[36:39], v[104:107], a[48:63]
	s_add_u32 m0, s48, 0xd3c0
	s_add_u32 s44, s44, 0x1800
	s_addc_u32 s45, s45, 0
	global_load_lds_dwordx4 v78, s[44:45]
	s_nop 0
	v_mfma_f32_32x32x16_f16 a[32:47], v[40:43], v[104:107], a[32:47]
	v_mfma_f32_32x32x16_f16 a[16:31], v[44:47], v[104:107], a[16:31]
	v_mfma_f32_32x32x16_f16 a[0:15], v[48:51], v[104:107], a[0:15]
	ds_read_b128 v[28:31], v98 offset:6144
	ds_read_b128 v[32:35], v98 offset:7168
	ds_read_b128 v[36:39], v98 offset:8192
	ds_read_b128 v[40:43], v98 offset:9216
	ds_read_b128 v[44:47], v98 offset:10240
	ds_read_b128 v[48:51], v98 offset:11264
	s_waitcnt lgkmcnt(6)
	s_nop 0
	v_mfma_f32_32x32x16_f16 a[80:95], v[4:7], v[108:111], a[80:95]
	s_waitcnt vmcnt(26)
	ds_write_b128 v81, v[132:135]
	ds_write_b128 v81, v[136:139] offset:1024
	ds_write_b128 v81, v[140:143] offset:2048
	ds_write_b128 v81, v[144:147] offset:3072
	s_nop 0
	v_mfma_f32_32x32x16_f16 a[64:79], v[8:11], v[108:111], a[64:79]
	ds_read_b128 v[52:55], v95
	ds_read_b128 v[56:59], v96
	ds_read_b128 v[60:63], v97
	ds_read_b128 v[0:3], v94
	v_mfma_f32_32x32x16_f16 a[48:63], v[12:15], v[108:111], a[48:63]
	s_waitcnt vmcnt(10)
	s_waitcnt lgkmcnt(8)
	s_barrier
	ds_read_b128 v[4:7], v84 offset:0
	ds_read_b128 v[8:11], v84 offset:1024
	ds_read_b128 v[12:15], v84 offset:2048
	s_nop 0
	v_mfma_f32_32x32x16_f16 a[32:47], v[16:19], v[108:111], a[32:47]
	ds_read_b128 v[16:19], v84 offset:3072
	v_mfma_f32_32x32x16_f16 a[16:31], v[20:23], v[108:111], a[16:31]
	ds_read_b128 v[20:23], v84 offset:4096
	v_mfma_f32_32x32x16_f16 a[0:15], v[24:27], v[108:111], a[0:15]
	ds_read_b128 v[24:27], v84 offset:5120
	v_mfma_f32_32x32x16_f16 a[80:95], v[28:31], v[112:115], a[80:95]
	s_add_u32 m0, s46, 0x103c0
	s_add_u32 s40, s40, 0x1800
	s_addc_u32 s41, s41, 0
	global_load_lds_dwordx4 v76, s[40:41]
	s_nop 0
	v_mfma_f32_32x32x16_f16 a[64:79], v[32:35], v[112:115], a[64:79]
	s_add_u32 m0, s47, 0x103c0
	s_add_u32 s42, s42, 0x1800
	s_addc_u32 s43, s43, 0
	global_load_lds_dwordx4 v77, s[42:43]
	s_nop 0
	v_mfma_f32_32x32x16_f16 a[48:63], v[36:39], v[112:115], a[48:63]
	s_add_u32 m0, s48, 0x103c0
	s_add_u32 s44, s44, 0x1800
	s_addc_u32 s45, s45, 0
	global_load_lds_dwordx4 v78, s[44:45]
	s_nop 0
	v_mfma_f32_32x32x16_f16 a[32:47], v[40:43], v[112:115], a[32:47]
	v_mfma_f32_32x32x16_f16 a[16:31], v[44:47], v[112:115], a[16:31]
	v_mfma_f32_32x32x16_f16 a[0:15], v[48:51], v[112:115], a[0:15]
	s_waitcnt lgkmcnt(6)
	ds_read_b128 v[28:31], v84 offset:6144
	ds_read_b128 v[32:35], v84 offset:7168
	ds_read_b128 v[36:39], v84 offset:8192
	ds_read_b128 v[40:43], v84 offset:9216
	ds_read_b128 v[44:47], v84 offset:10240
	ds_read_b128 v[48:51], v84 offset:11264
	s_waitcnt lgkmcnt(6)
	v_mfma_f32_32x32x16_f16 a[80:95], v[4:7], v[52:55], a[80:95]
	v_mfma_f32_32x32x16_f16 a[64:79], v[8:11], v[52:55], a[64:79]
	v_mfma_f32_32x32x16_f16 a[48:63], v[12:15], v[52:55], a[48:63]
	s_waitcnt vmcnt(6)
	s_waitcnt lgkmcnt(0)
	s_barrier
	ds_read_b128 v[4:7], v84 offset:12288
	ds_read_b128 v[8:11], v84 offset:13312
	ds_read_b128 v[12:15], v84 offset:14336
	s_nop 0
	v_mfma_f32_32x32x16_f16 a[32:47], v[16:19], v[52:55], a[32:47]
	ds_read_b128 v[16:19], v84 offset:15360
	v_mfma_f32_32x32x16_f16 a[16:31], v[20:23], v[52:55], a[16:31]
	ds_read_b128 v[20:23], v84 offset:16384
	v_mfma_f32_32x32x16_f16 a[0:15], v[24:27], v[52:55], a[0:15]
	ds_read_b128 v[24:27], v84 offset:17408
	v_mfma_f32_32x32x16_f16 a[80:95], v[28:31], v[56:59], a[80:95]
	s_add_u32 m0, s46, 0x0
	s_add_u32 s40, s40, 0x1800
	s_addc_u32 s41, s41, 0
	global_load_lds_dwordx4 v76, s[40:41]
	v_mfma_f32_32x32x16_f16 a[64:79], v[32:35], v[56:59], a[64:79]
	s_add_u32 m0, s47, 0x0
	s_add_u32 s42, s42, s49
	s_addc_u32 s43, s43, 0
	global_load_lds_dwordx4 v77, s[42:43]
	s_nop 0
	v_mfma_f32_32x32x16_f16 a[48:63], v[36:39], v[56:59], a[48:63]
	s_add_u32 m0, s48, 0x0
	s_add_u32 s44, s44, 0xc00
	s_addc_u32 s45, s45, 0
	global_load_lds_dwordx4 v78, s[44:45]
	v_mfma_f32_32x32x16_f16 a[32:47], v[40:43], v[56:59], a[32:47]
	v_mfma_f32_32x32x16_f16 a[16:31], v[44:47], v[56:59], a[16:31]
	v_mfma_f32_32x32x16_f16 a[0:15], v[48:51], v[56:59], a[0:15]
	ds_read_b128 v[28:31], v84 offset:18432
	ds_read_b128 v[32:35], v84 offset:19456
	ds_read_b128 v[36:39], v84 offset:20480
	ds_read_b128 v[40:43], v84 offset:21504
	ds_read_b128 v[44:47], v84 offset:22528
	ds_read_b128 v[48:51], v84 offset:23552
	s_waitcnt lgkmcnt(6)
	s_nop 0
	v_mfma_f32_32x32x16_f16 a[80:95], v[4:7], v[60:63], a[80:95]
	s_waitcnt vmcnt(22)
	ds_write_b128 v81, v[148:151]
	ds_write_b128 v81, v[152:155] offset:1024
	ds_write_b128 v81, v[156:159] offset:2048
	ds_write_b128 v81, v[72:75] offset:3072
	s_nop 0
	v_mfma_f32_32x32x16_f16 a[64:79], v[8:11], v[60:63], a[64:79]
	ds_read_b128 v[100:103], v95
	ds_read_b128 v[104:107], v96
	ds_read_b128 v[108:111], v97
	ds_read_b128 v[112:115], v94
	v_mfma_f32_32x32x16_f16 a[48:63], v[12:15], v[60:63], a[48:63]
	s_waitcnt vmcnt(6)
	s_waitcnt lgkmcnt(8)
	s_barrier
	ds_read_b128 v[4:7], v84 offset:54208
	ds_read_b128 v[8:11], v84 offset:55232
	ds_read_b128 v[12:15], v84 offset:56256
	s_nop 0
	v_mfma_f32_32x32x16_f16 a[32:47], v[16:19], v[60:63], a[32:47]
	ds_read_b128 v[16:19], v84 offset:57280
	v_mfma_f32_32x32x16_f16 a[16:31], v[20:23], v[60:63], a[16:31]
	ds_read_b128 v[20:23], v84 offset:58304
	v_mfma_f32_32x32x16_f16 a[0:15], v[24:27], v[60:63], a[0:15]
	ds_read_b128 v[24:27], v84 offset:59328
	v_mfma_f32_32x32x16_f16 a[80:95], v[28:31], v[0:3], a[80:95]
	v_mfma_f32_32x32x16_f16 a[64:79], v[32:35], v[0:3], a[64:79]
	v_mfma_f32_32x32x16_f16 a[48:63], v[36:39], v[0:3], a[48:63]
	v_mfma_f32_32x32x16_f16 a[32:47], v[40:43], v[0:3], a[32:47]
	v_mfma_f32_32x32x16_f16 a[16:31], v[44:47], v[0:3], a[16:31]
	v_mfma_f32_32x32x16_f16 a[0:15], v[48:51], v[0:3], a[0:15]
	s_waitcnt lgkmcnt(6)
	ds_read_b128 v[28:31], v84 offset:60352
	ds_read_b128 v[32:35], v84 offset:61376
	ds_read_b128 v[36:39], v84 offset:62400
	ds_read_b128 v[40:43], v84 offset:63424
	ds_read_b128 v[44:47], v84 offset:64448
	ds_read_b128 v[48:51], v84 offset:65472
	s_waitcnt lgkmcnt(6)
	v_mfma_f32_32x32x16_f16 a[80:95], v[4:7], v[100:103], a[80:95]
	v_mfma_f32_32x32x16_f16 a[64:79], v[8:11], v[100:103], a[64:79]
	v_mfma_f32_32x32x16_f16 a[48:63], v[12:15], v[100:103], a[48:63]
	s_waitcnt vmcnt(3)
	s_waitcnt lgkmcnt(0)
	s_barrier
	ds_read_b128 v[4:7], v98
	ds_read_b128 v[8:11], v98 offset:1024
	ds_read_b128 v[12:15], v98 offset:2048
	s_nop 0
	v_mfma_f32_32x32x16_f16 a[32:47], v[16:19], v[100:103], a[32:47]
	ds_read_b128 v[16:19], v98 offset:3072
	v_mfma_f32_32x32x16_f16 a[16:31], v[20:23], v[100:103], a[16:31]
	ds_read_b128 v[20:23], v98 offset:4096
	v_mfma_f32_32x32x16_f16 a[0:15], v[24:27], v[100:103], a[0:15]
	ds_read_b128 v[24:27], v98 offset:5120
	v_mfma_f32_32x32x16_f16 a[80:95], v[28:31], v[104:107], a[80:95]
	v_mfma_f32_32x32x16_f16 a[64:79], v[32:35], v[104:107], a[64:79]
	v_mfma_f32_32x32x16_f16 a[48:63], v[36:39], v[104:107], a[48:63]
	v_mfma_f32_32x32x16_f16 a[32:47], v[40:43], v[104:107], a[32:47]
	v_mfma_f32_32x32x16_f16 a[16:31], v[44:47], v[104:107], a[16:31]
	v_mfma_f32_32x32x16_f16 a[0:15], v[48:51], v[104:107], a[0:15]
	ds_read_b128 v[28:31], v98 offset:6144
	ds_read_b128 v[32:35], v98 offset:7168
	ds_read_b128 v[36:39], v98 offset:8192
	ds_read_b128 v[40:43], v98 offset:9216
	ds_read_b128 v[44:47], v98 offset:10240
	ds_read_b128 v[48:51], v98 offset:11264
	s_waitcnt lgkmcnt(6)
	s_nop 0
	v_mfma_f32_32x32x16_f16 a[80:95], v[4:7], v[108:111], a[80:95]
	s_waitcnt vmcnt(12)
	ds_write_b128 v81, v[116:119]
	ds_write_b128 v81, v[120:123] offset:1024
	ds_write_b128 v81, v[124:127] offset:2048
	ds_write_b128 v81, v[128:131] offset:3072
	s_nop 0
	v_mfma_f32_32x32x16_f16 a[64:79], v[8:11], v[108:111], a[64:79]
	ds_read_b128 v[0:3], v94
	v_mfma_f32_32x32x16_f16 a[48:63], v[12:15], v[108:111], a[48:63]
	s_waitcnt vmcnt(0)
	s_waitcnt lgkmcnt(5)
	s_barrier
	ds_read_b128 v[4:7], v84 offset:0
	ds_read_b128 v[8:11], v84 offset:1024
	ds_read_b128 v[12:15], v84 offset:2048
	s_nop 0
	v_mfma_f32_32x32x16_f16 a[32:47], v[16:19], v[108:111], a[32:47]
	ds_read_b128 v[16:19], v84 offset:3072
	v_mfma_f32_32x32x16_f16 a[16:31], v[20:23], v[108:111], a[16:31]
	ds_read_b128 v[20:23], v84 offset:4096
	v_mfma_f32_32x32x16_f16 a[0:15], v[24:27], v[108:111], a[0:15]
	ds_read_b128 v[24:27], v84 offset:5120
	v_mfma_f32_32x32x16_f16 a[80:95], v[28:31], v[112:115], a[80:95]
	v_mfma_f32_32x32x16_f16 a[64:79], v[32:35], v[112:115], a[64:79]
	v_mfma_f32_32x32x16_f16 a[48:63], v[36:39], v[112:115], a[48:63]
	v_mfma_f32_32x32x16_f16 a[32:47], v[40:43], v[112:115], a[32:47]
	v_mfma_f32_32x32x16_f16 a[16:31], v[44:47], v[112:115], a[16:31]
	v_mfma_f32_32x32x16_f16 a[0:15], v[48:51], v[112:115], a[0:15]
	s_waitcnt lgkmcnt(0)
	v_mfma_f32_32x32x16_f16 a[80:95], v[4:7], v[0:3], a[80:95]
	v_mfma_f32_32x32x16_f16 a[16:31], v[20:23], v[0:3], a[16:31]
	v_lshlrev_b32_e32 v22, 4, v85
	v_mfma_f32_32x32x16_f16 a[64:79], v[8:11], v[0:3], a[64:79]
	v_mfma_f32_32x32x16_f16 a[48:63], v[12:15], v[0:3], a[48:63]
	s_nop 7
	v_accvgpr_read_b32 v13, a88
	v_mfma_f32_32x32x16_f16 a[32:47], v[16:19], v[0:3], a[32:47]
	v_accvgpr_read_b32 v17, a92
	v_mfma_f32_32x32x16_f16 a[0:15], v[24:27], v[0:3], a[0:15]
	ds_read_b128 v[2:5], v22 offset:53248
	ds_read_b128 v[6:9], v22 offset:53280
	v_accvgpr_read_b32 v1, a80
	v_lshlrev_b32_e32 v0, 4, v92
	s_waitcnt lgkmcnt(1)
	v_add_f32_e32 v1, v1, v2
	v_accvgpr_read_b32 v2, a81
	v_add_f32_e32 v2, v3, v2
	v_max_f32_e32 v10, 0, v2
	v_accvgpr_read_b32 v2, a82
	v_add_f32_e32 v2, v4, v2
	v_max_f32_e32 v11, 0, v2
	v_accvgpr_read_b32 v2, a83
	v_add_f32_e32 v2, v5, v2
	v_max_f32_e32 v12, 0, v2
	v_accvgpr_read_b32 v2, a84
	s_waitcnt lgkmcnt(0)
	v_add_f32_e32 v2, v2, v6
	v_max_f32_e32 v6, 0, v2
	v_accvgpr_read_b32 v2, a85
	v_add_f32_e32 v2, v7, v2
	v_max_f32_e32 v7, 0, v2
	v_accvgpr_read_b32 v2, a86
	v_add_f32_e32 v2, v8, v2
	v_max_f32_e32 v8, 0, v2
	v_accvgpr_read_b32 v2, a87
	v_add_f32_e32 v2, v9, v2
	v_max_f32_e32 v9, 0, v2
	ds_read_b128 v[2:5], v22 offset:53312
	v_max_f32_e32 v1, 0, v1
	s_waitcnt lgkmcnt(0)
	v_add_f32_e32 v2, v13, v2
	v_max_f32_e32 v13, 0, v2
	v_accvgpr_read_b32 v2, a89
	v_add_f32_e32 v2, v3, v2
	v_max_f32_e32 v14, 0, v2
	v_accvgpr_read_b32 v2, a90
	v_add_f32_e32 v2, v4, v2
	v_max_f32_e32 v15, 0, v2
	v_accvgpr_read_b32 v2, a91
	v_add_f32_e32 v2, v5, v2
	v_max_f32_e32 v16, 0, v2
	ds_read_b128 v[2:5], v22 offset:53344
	s_waitcnt lgkmcnt(0)
	v_add_f32_e32 v2, v17, v2
	v_max_f32_e32 v17, 0, v2
	v_accvgpr_read_b32 v2, a93
	v_add_f32_e32 v2, v3, v2
	v_max_f32_e32 v18, 0, v2
	v_accvgpr_read_b32 v2, a94
	v_add_f32_e32 v2, v4, v2
	v_max_f32_e32 v19, 0, v2
	v_accvgpr_read_b32 v2, a95
	v_add_f32_e32 v2, v5, v2
	v_cvt_pk_f16_f32 v5, v8, v9
	v_cvt_pk_f16_f32 v4, v6, v7
	ds_read_b128 v[6:9], v0 offset:40960
	v_max_f32_e32 v20, 0, v2
	v_cvt_pk_f16_f32 v3, v11, v12
	v_cvt_pk_f16_f32 v2, v1, v10
	v_accvgpr_read_b32 v1, a64
	s_waitcnt lgkmcnt(0)
	v_mfma_f32_32x32x16_f16 a[80:95], v[6:9], v[2:5], 0
	ds_read_b128 v[6:9], v0 offset:41984
	v_cvt_pk_f16_f32 v5, v19, v20
	v_cvt_pk_f16_f32 v4, v17, v18
	v_cvt_pk_f16_f32 v3, v15, v16
	v_cvt_pk_f16_f32 v2, v13, v14
	v_accvgpr_read_b32 v13, a72
	v_accvgpr_read_b32 v17, a76
	s_waitcnt lgkmcnt(0)
	v_mfma_f32_32x32x16_f16 a[80:95], v[6:9], v[2:5], a[80:95]
	ds_read_b128 v[2:5], v22 offset:53376
	v_accvgpr_read_b32 v9, a68
	s_waitcnt lgkmcnt(0)
	v_add_f32_e32 v1, v1, v2
	v_accvgpr_read_b32 v2, a65
	v_add_f32_e32 v2, v3, v2
	v_max_f32_e32 v6, 0, v2
	v_accvgpr_read_b32 v2, a66
	v_add_f32_e32 v2, v4, v2
	v_max_f32_e32 v7, 0, v2
	v_accvgpr_read_b32 v2, a67
	v_add_f32_e32 v2, v5, v2
	v_max_f32_e32 v8, 0, v2
	ds_read_b128 v[2:5], v22 offset:53408
	v_max_f32_e32 v1, 0, v1
	s_waitcnt lgkmcnt(0)
	v_add_f32_e32 v2, v9, v2
	v_max_f32_e32 v9, 0, v2
	v_accvgpr_read_b32 v2, a69
	v_add_f32_e32 v2, v3, v2
	v_max_f32_e32 v10, 0, v2
	v_accvgpr_read_b32 v2, a70
	v_add_f32_e32 v2, v4, v2
	v_max_f32_e32 v11, 0, v2
	v_accvgpr_read_b32 v2, a71
	v_add_f32_e32 v2, v5, v2
	v_max_f32_e32 v12, 0, v2
	ds_read_b128 v[2:5], v22 offset:53440
	s_waitcnt lgkmcnt(0)
	v_add_f32_e32 v2, v13, v2
	v_max_f32_e32 v13, 0, v2
	v_accvgpr_read_b32 v2, a73
	v_add_f32_e32 v2, v3, v2
	v_max_f32_e32 v14, 0, v2
	v_accvgpr_read_b32 v2, a74
	v_add_f32_e32 v2, v4, v2
	v_max_f32_e32 v15, 0, v2
	v_accvgpr_read_b32 v2, a75
	v_add_f32_e32 v2, v5, v2
	v_max_f32_e32 v16, 0, v2
	ds_read_b128 v[2:5], v22 offset:53472
	s_waitcnt lgkmcnt(0)
	v_add_f32_e32 v2, v17, v2
	v_max_f32_e32 v17, 0, v2
	v_accvgpr_read_b32 v2, a77
	v_add_f32_e32 v2, v3, v2
	v_max_f32_e32 v18, 0, v2
	v_accvgpr_read_b32 v2, a78
	v_add_f32_e32 v2, v4, v2
	v_max_f32_e32 v19, 0, v2
	v_accvgpr_read_b32 v2, a79
	v_add_f32_e32 v2, v5, v2
	v_max_f32_e32 v20, 0, v2
	v_cvt_pk_f16_f32 v4, v9, v10
	v_cvt_pk_f16_f32 v3, v7, v8
	v_cvt_pk_f16_f32 v2, v1, v6
	ds_read_b128 v[6:9], v0 offset:43008
	v_cvt_pk_f16_f32 v5, v11, v12
	v_accvgpr_read_b32 v1, a48
	s_waitcnt lgkmcnt(0)
	v_mfma_f32_32x32x16_f16 a[80:95], v[6:9], v[2:5], a[80:95]
	ds_read_b128 v[6:9], v0 offset:44032
	v_cvt_pk_f16_f32 v5, v19, v20
	v_cvt_pk_f16_f32 v4, v17, v18
	v_cvt_pk_f16_f32 v3, v15, v16
	v_cvt_pk_f16_f32 v2, v13, v14
	v_accvgpr_read_b32 v13, a56
	v_accvgpr_read_b32 v17, a60
	s_waitcnt lgkmcnt(0)
	v_mfma_f32_32x32x16_f16 a[80:95], v[6:9], v[2:5], a[80:95]
	ds_read_b128 v[2:5], v22 offset:53504
	v_accvgpr_read_b32 v9, a52
	s_waitcnt lgkmcnt(0)
	v_add_f32_e32 v1, v1, v2
	v_accvgpr_read_b32 v2, a49
	v_add_f32_e32 v2, v3, v2
	v_max_f32_e32 v6, 0, v2
	v_accvgpr_read_b32 v2, a50
	v_add_f32_e32 v2, v4, v2
	v_max_f32_e32 v7, 0, v2
	v_accvgpr_read_b32 v2, a51
	v_add_f32_e32 v2, v5, v2
	v_max_f32_e32 v8, 0, v2
	ds_read_b128 v[2:5], v22 offset:53536
	v_max_f32_e32 v1, 0, v1
	s_waitcnt lgkmcnt(0)
	v_add_f32_e32 v2, v9, v2
	v_max_f32_e32 v9, 0, v2
	v_accvgpr_read_b32 v2, a53
	v_add_f32_e32 v2, v3, v2
	v_max_f32_e32 v10, 0, v2
	v_accvgpr_read_b32 v2, a54
	v_add_f32_e32 v2, v4, v2
	v_max_f32_e32 v11, 0, v2
	v_accvgpr_read_b32 v2, a55
	v_add_f32_e32 v2, v5, v2
	v_max_f32_e32 v12, 0, v2
	ds_read_b128 v[2:5], v22 offset:53568
	s_waitcnt lgkmcnt(0)
	v_add_f32_e32 v2, v13, v2
	v_max_f32_e32 v13, 0, v2
	v_accvgpr_read_b32 v2, a57
	v_add_f32_e32 v2, v3, v2
	v_max_f32_e32 v14, 0, v2
	v_accvgpr_read_b32 v2, a58
	v_add_f32_e32 v2, v4, v2
	v_max_f32_e32 v15, 0, v2
	v_accvgpr_read_b32 v2, a59
	v_add_f32_e32 v2, v5, v2
	v_max_f32_e32 v16, 0, v2
	ds_read_b128 v[2:5], v22 offset:53600
	s_waitcnt lgkmcnt(0)
	v_add_f32_e32 v2, v17, v2
	v_max_f32_e32 v17, 0, v2
	v_accvgpr_read_b32 v2, a61
	v_add_f32_e32 v2, v3, v2
	v_max_f32_e32 v18, 0, v2
	v_accvgpr_read_b32 v2, a62
	v_add_f32_e32 v2, v4, v2
	v_max_f32_e32 v19, 0, v2
	v_accvgpr_read_b32 v2, a63
	v_add_f32_e32 v2, v5, v2
	v_max_f32_e32 v20, 0, v2
	v_cvt_pk_f16_f32 v4, v9, v10
	v_cvt_pk_f16_f32 v3, v7, v8
	v_cvt_pk_f16_f32 v2, v1, v6
	ds_read_b128 v[6:9], v0 offset:45056
	v_cvt_pk_f16_f32 v5, v11, v12
	v_accvgpr_read_b32 v1, a32
	s_waitcnt lgkmcnt(0)
	v_mfma_f32_32x32x16_f16 a[80:95], v[6:9], v[2:5], a[80:95]
	ds_read_b128 v[6:9], v0 offset:46080
	v_cvt_pk_f16_f32 v5, v19, v20
	v_cvt_pk_f16_f32 v4, v17, v18
	v_cvt_pk_f16_f32 v3, v15, v16
	v_cvt_pk_f16_f32 v2, v13, v14
	v_accvgpr_read_b32 v13, a40
	v_accvgpr_read_b32 v17, a44
	s_waitcnt lgkmcnt(0)
	v_mfma_f32_32x32x16_f16 a[80:95], v[6:9], v[2:5], a[80:95]
	ds_read_b128 v[2:5], v22 offset:53632
	v_accvgpr_read_b32 v9, a36
	s_waitcnt lgkmcnt(0)
	v_add_f32_e32 v1, v1, v2
	v_accvgpr_read_b32 v2, a33
	v_add_f32_e32 v2, v3, v2
	v_max_f32_e32 v6, 0, v2
	v_accvgpr_read_b32 v2, a34
	v_add_f32_e32 v2, v4, v2
	v_max_f32_e32 v7, 0, v2
	v_accvgpr_read_b32 v2, a35
	v_add_f32_e32 v2, v5, v2
	v_max_f32_e32 v8, 0, v2
	ds_read_b128 v[2:5], v22 offset:53664
	v_max_f32_e32 v1, 0, v1
	s_waitcnt lgkmcnt(0)
	v_add_f32_e32 v2, v9, v2
	v_max_f32_e32 v9, 0, v2
	v_accvgpr_read_b32 v2, a37
	v_add_f32_e32 v2, v3, v2
	v_max_f32_e32 v10, 0, v2
	v_accvgpr_read_b32 v2, a38
	v_add_f32_e32 v2, v4, v2
	v_max_f32_e32 v11, 0, v2
	v_accvgpr_read_b32 v2, a39
	v_add_f32_e32 v2, v5, v2
	v_max_f32_e32 v12, 0, v2
	ds_read_b128 v[2:5], v22 offset:53696
	s_waitcnt lgkmcnt(0)
	v_add_f32_e32 v2, v13, v2
	v_max_f32_e32 v13, 0, v2
	v_accvgpr_read_b32 v2, a41
	v_add_f32_e32 v2, v3, v2
	v_max_f32_e32 v14, 0, v2
	v_accvgpr_read_b32 v2, a42
	v_add_f32_e32 v2, v4, v2
	v_max_f32_e32 v15, 0, v2
	v_accvgpr_read_b32 v2, a43
	v_add_f32_e32 v2, v5, v2
	v_max_f32_e32 v16, 0, v2
	ds_read_b128 v[2:5], v22 offset:53728
	s_waitcnt lgkmcnt(0)
	v_add_f32_e32 v2, v17, v2
	v_max_f32_e32 v17, 0, v2
	v_accvgpr_read_b32 v2, a45
	v_add_f32_e32 v2, v3, v2
	v_max_f32_e32 v18, 0, v2
	v_accvgpr_read_b32 v2, a46
	v_add_f32_e32 v2, v4, v2
	v_max_f32_e32 v19, 0, v2
	v_accvgpr_read_b32 v2, a47
	v_add_f32_e32 v2, v5, v2
	v_max_f32_e32 v20, 0, v2
	v_cvt_pk_f16_f32 v4, v9, v10
	v_cvt_pk_f16_f32 v3, v7, v8
	v_cvt_pk_f16_f32 v2, v1, v6
	ds_read_b128 v[6:9], v0 offset:47104
	v_cvt_pk_f16_f32 v5, v11, v12
	v_accvgpr_read_b32 v1, a16
	s_waitcnt lgkmcnt(0)
	v_mfma_f32_32x32x16_f16 a[32:47], v[6:9], v[2:5], 0
	ds_read_b128 v[6:9], v0 offset:48128
	v_cvt_pk_f16_f32 v5, v19, v20
	v_cvt_pk_f16_f32 v4, v17, v18
	v_cvt_pk_f16_f32 v3, v15, v16
	v_cvt_pk_f16_f32 v2, v13, v14
	v_accvgpr_read_b32 v13, a24
	v_accvgpr_read_b32 v17, a28
	s_waitcnt lgkmcnt(0)
	v_mfma_f32_32x32x16_f16 a[32:47], v[6:9], v[2:5], a[32:47]
	ds_read_b128 v[2:5], v22 offset:53760
	v_accvgpr_read_b32 v9, a20
	s_waitcnt lgkmcnt(0)
	v_add_f32_e32 v1, v1, v2
	v_accvgpr_read_b32 v2, a17
	v_add_f32_e32 v2, v3, v2
	v_max_f32_e32 v6, 0, v2
	v_accvgpr_read_b32 v2, a18
	v_add_f32_e32 v2, v4, v2
	v_max_f32_e32 v7, 0, v2
	v_accvgpr_read_b32 v2, a19
	v_add_f32_e32 v2, v5, v2
	v_max_f32_e32 v8, 0, v2
	ds_read_b128 v[2:5], v22 offset:53792
	v_max_f32_e32 v1, 0, v1
	s_waitcnt lgkmcnt(0)
	v_add_f32_e32 v2, v9, v2
	v_max_f32_e32 v9, 0, v2
	v_accvgpr_read_b32 v2, a21
	v_add_f32_e32 v2, v3, v2
	v_max_f32_e32 v10, 0, v2
	v_accvgpr_read_b32 v2, a22
	v_add_f32_e32 v2, v4, v2
	v_max_f32_e32 v11, 0, v2
	v_accvgpr_read_b32 v2, a23
	v_add_f32_e32 v2, v5, v2
	v_max_f32_e32 v12, 0, v2
	ds_read_b128 v[2:5], v22 offset:53824
	s_waitcnt lgkmcnt(0)
	v_add_f32_e32 v2, v13, v2
	v_max_f32_e32 v13, 0, v2
	v_accvgpr_read_b32 v2, a25
	v_add_f32_e32 v2, v3, v2
	v_max_f32_e32 v14, 0, v2
	v_accvgpr_read_b32 v2, a26
	v_add_f32_e32 v2, v4, v2
	v_max_f32_e32 v15, 0, v2
	v_accvgpr_read_b32 v2, a27
	v_add_f32_e32 v2, v5, v2
	v_max_f32_e32 v16, 0, v2
	ds_read_b128 v[2:5], v22 offset:53856
	s_waitcnt lgkmcnt(0)
	v_add_f32_e32 v2, v17, v2
	v_max_f32_e32 v17, 0, v2
	v_accvgpr_read_b32 v2, a29
	v_add_f32_e32 v2, v3, v2
	v_max_f32_e32 v18, 0, v2
	v_accvgpr_read_b32 v2, a30
	v_add_f32_e32 v2, v4, v2
	v_max_f32_e32 v19, 0, v2
	v_accvgpr_read_b32 v2, a31
	v_add_f32_e32 v2, v5, v2
	v_max_f32_e32 v20, 0, v2
	v_cvt_pk_f16_f32 v4, v9, v10
	v_cvt_pk_f16_f32 v3, v7, v8
	v_cvt_pk_f16_f32 v2, v1, v6
	ds_read_b128 v[6:9], v0 offset:49152
	v_cvt_pk_f16_f32 v5, v11, v12
	v_accvgpr_read_b32 v1, a0
	s_waitcnt lgkmcnt(0)
	v_mfma_f32_32x32x16_f16 a[32:47], v[6:9], v[2:5], a[32:47]
	ds_read_b128 v[6:9], v0 offset:50176
	v_cvt_pk_f16_f32 v5, v19, v20
	v_cvt_pk_f16_f32 v4, v17, v18
	v_cvt_pk_f16_f32 v3, v15, v16
	v_cvt_pk_f16_f32 v2, v13, v14
	v_accvgpr_read_b32 v13, a8
	v_accvgpr_read_b32 v17, a12
	s_waitcnt lgkmcnt(0)
	v_mfma_f32_32x32x16_f16 a[32:47], v[6:9], v[2:5], a[32:47]
	ds_read_b128 v[2:5], v22 offset:53888
	v_accvgpr_read_b32 v9, a4
	s_waitcnt lgkmcnt(0)
	v_add_f32_e32 v1, v1, v2
	v_accvgpr_read_b32 v2, a1
	v_add_f32_e32 v2, v3, v2
	v_max_f32_e32 v6, 0, v2
	v_accvgpr_read_b32 v2, a2
	v_add_f32_e32 v2, v4, v2
	v_max_f32_e32 v7, 0, v2
	v_accvgpr_read_b32 v2, a3
	v_add_f32_e32 v2, v5, v2
	v_max_f32_e32 v8, 0, v2
	ds_read_b128 v[2:5], v22 offset:53920
	v_max_f32_e32 v1, 0, v1
	s_waitcnt lgkmcnt(0)
	v_add_f32_e32 v2, v9, v2
	v_max_f32_e32 v9, 0, v2
	v_accvgpr_read_b32 v2, a5
	v_add_f32_e32 v2, v3, v2
	v_max_f32_e32 v10, 0, v2
	v_accvgpr_read_b32 v2, a6
	v_add_f32_e32 v2, v4, v2
	v_max_f32_e32 v11, 0, v2
	v_accvgpr_read_b32 v2, a7
	v_add_f32_e32 v2, v5, v2
	v_max_f32_e32 v12, 0, v2
	ds_read_b128 v[2:5], v22 offset:53952
	s_waitcnt lgkmcnt(0)
	v_add_f32_e32 v2, v13, v2
	v_max_f32_e32 v13, 0, v2
	v_accvgpr_read_b32 v2, a9
	v_add_f32_e32 v2, v3, v2
	v_max_f32_e32 v14, 0, v2
	v_accvgpr_read_b32 v2, a10
	v_add_f32_e32 v2, v4, v2
	v_max_f32_e32 v15, 0, v2
	v_accvgpr_read_b32 v2, a11
	v_add_f32_e32 v2, v5, v2
	v_max_f32_e32 v16, 0, v2
	ds_read_b128 v[2:5], v22 offset:53984
	s_waitcnt lgkmcnt(0)
	v_add_f32_e32 v2, v17, v2
	v_max_f32_e32 v17, 0, v2
	v_accvgpr_read_b32 v2, a13
	v_add_f32_e32 v2, v3, v2
	v_max_f32_e32 v18, 0, v2
	v_accvgpr_read_b32 v2, a14
	v_add_f32_e32 v2, v4, v2
	v_max_f32_e32 v19, 0, v2
	v_accvgpr_read_b32 v2, a15
	v_add_f32_e32 v2, v5, v2
	v_max_f32_e32 v20, 0, v2
	v_cvt_pk_f16_f32 v4, v9, v10
	v_cvt_pk_f16_f32 v3, v7, v8
	v_cvt_pk_f16_f32 v2, v1, v6
	ds_read_b128 v[6:9], v0 offset:51200
	v_cvt_pk_f16_f32 v5, v11, v12
	s_waitcnt lgkmcnt(0)
	s_nop 0
	v_mfma_f32_32x32x16_f16 a[32:47], v[6:9], v[2:5], a[32:47]
	ds_read_b128 v[6:9], v0 offset:52224
	v_cvt_pk_f16_f32 v5, v19, v20
	v_cvt_pk_f16_f32 v4, v17, v18
	v_cvt_pk_f16_f32 v3, v15, v16
	v_cvt_pk_f16_f32 v2, v13, v14
	s_waitcnt lgkmcnt(0)
	s_nop 0
	v_mfma_f32_32x32x16_f16 a[32:47], v[6:9], v[2:5], a[32:47]
	s_and_saveexec_b64 s[2:3], s[0:1]
	s_cbranch_execz .LBB3_39
	v_accvgpr_read_b32 v0, a80
	v_accvgpr_read_b32 v6, a86
	v_accvgpr_read_b32 v7, a87
	v_accvgpr_read_b32 v8, a88
	v_accvgpr_read_b32 v9, a89
	v_accvgpr_read_b32 v10, a90
	v_accvgpr_read_b32 v11, a91
	v_accvgpr_read_b32 v12, a92
	v_accvgpr_read_b32 v13, a93
	v_accvgpr_read_b32 v14, a94
	v_accvgpr_read_b32 v15, a95
	v_accvgpr_read_b32 v6, a32
	v_accvgpr_read_b32 v14, a40
	v_accvgpr_read_b32 v15, a41
	v_accvgpr_read_b32 v16, a42
	v_accvgpr_read_b32 v17, a43
	v_accvgpr_read_b32 v18, a44
	v_accvgpr_read_b32 v19, a45
	v_accvgpr_read_b32 v20, a46
	v_accvgpr_read_b32 v21, a47
	ds_read_b128 v[14:17], v22 offset:54016
	ds_read_b128 v[18:21], v22 offset:54080
	v_accvgpr_read_b32 v12, a38
	v_accvgpr_read_b32 v13, a39
	v_lshlrev_b32_e32 v24, 2, v85
	v_accvgpr_read_b32 v1, a81
	v_accvgpr_read_b32 v7, a33
	v_mad_i64_i32 v[12:13], s[0:1], v80, 40, s[18:19]
	v_ashrrev_i32_e32 v25, 31, v24
	v_accvgpr_read_b32 v3, a83
	v_accvgpr_read_b32 v9, a35
	v_lshl_add_u64 v[22:23], v[24:25], 2, v[12:13]
	v_mov_b32_e32 v25, v1
	s_waitcnt lgkmcnt(1)
	v_mov_b32_e32 v27, v15
	v_mov_b32_e32 v1, v7
	s_waitcnt lgkmcnt(0)
	v_mov_b32_e32 v15, v19
	v_accvgpr_read_b32 v2, a82
	v_accvgpr_read_b32 v8, a34
	v_pk_add_f32 v[0:1], v[0:1], v[14:15]
	v_mov_b32_e32 v7, v3
	v_mov_b32_e32 v15, v17
	v_mov_b32_e32 v3, v9
	v_mov_b32_e32 v17, v21
	v_mov_b32_e32 v24, v6
	v_mov_b32_e32 v26, v18
	v_mov_b32_e32 v6, v8
	v_mov_b32_e32 v14, v20
	v_pk_add_f32 v[2:3], v[2:3], v[16:17]
	v_pk_add_f32 v[24:25], v[24:25], v[26:27]
	s_waitcnt vmcnt(0)
	v_pk_mul_f32 v[0:1], v[82:83], v[0:1]
	v_pk_add_f32 v[6:7], v[6:7], v[14:15]
	v_pk_mul_f32 v[2:3], v[82:83], v[2:3]
	v_accvgpr_read_b32 v4, a84
	v_accvgpr_read_b32 v5, a85
	v_accvgpr_read_b32 v10, a36
	v_accvgpr_read_b32 v11, a37
	v_pk_fma_f32 v[0:1], v[82:83], v[24:25], v[0:1] op_sel:[1,0,0] op_sel_hi:[0,1,1]
	v_pk_fma_f32 v[2:3], v[82:83], v[6:7], v[2:3] op_sel:[1,0,0] op_sel_hi:[0,1,1]
	v_cmp_eq_u32_e32 vcc, 0, v85
	global_store_dwordx4 v[22:23], v[0:3], off
	s_and_b64 exec, exec, vcc
	s_cbranch_execz .LBB3_39
	s_mov_b32 s0, 0xd000
	v_add_u32_e64 v0, s0, 0
	ds_read2_b64 v[0:3], v0 offset0:100 offset1:108
	v_mov_b32_e32 v9, v5
	v_mov_b32_e32 v5, v11
	v_mov_b32_e32 v8, v10
	v_pk_mov_b32 v[6:7], v[82:83], v[82:83] op_sel:[1,0]
	s_waitcnt lgkmcnt(0)
	v_mov_b32_e32 v15, v1
	v_mov_b32_e32 v1, v3
	v_mov_b32_e32 v14, v2
	v_pk_add_f32 v[0:1], v[4:5], v[0:1]
	v_pk_add_f32 v[8:9], v[8:9], v[14:15]
	v_pk_mul_f32 v[0:1], v[82:83], v[0:1]
	s_nop 0
	v_pk_fma_f32 v[0:1], v[6:7], v[8:9], v[0:1]
	global_store_dwordx2 v[12:13], v[0:1], off offset:32
